# speedup vs baseline: 1.0199x; 1.0199x over previous
_Z11proj_kernelPKfS0_S0_PKDF16_S0_S0_S0_PDF16_S3_S3_Pj:
	s_ashr_i32 s12, s2, 6
	s_load_dwordx8 s[4:11], s[0:1], 0x0
	s_cmp_gt_u32 s2, 63
	s_cselect_b64 s[22:23], -1, 0
	s_cmp_lg_u32 s12, 1
	s_cselect_b64 s[18:19], -1, 0
	s_cmp_eq_u32 s12, 1
	s_cselect_b64 s[20:21], -1, 0
	s_and_b64 s[14:15], s[20:21], exec
	s_waitcnt lgkmcnt(0)
	s_cselect_b32 s14, s6, s8
	s_cselect_b32 s15, s7, s9
	s_ashr_i32 s13, s12, 31
	s_lshl_b32 s28, s2, 7
	s_lshl_b64 s[6:7], s[12:13], 19
	s_and_b32 s3, s28, 0x1f80
	s_cmp_lt_u32 s2, 64
	s_cselect_b64 vcc, -1, 0
	v_lshrrev_b32_e32 v1, 2, v0
	v_or_b32_e32 v2, s3, v1
	s_and_b64 s[8:9], vcc, exec
	s_cselect_b32 s25, s5, s15
	s_cselect_b32 s24, s4, s14
	v_lshlrev_b32_e32 v2, 11, v2
	v_mov_b32_e32 v3, 0
	v_lshlrev_b32_e32 v6, 5, v0
	s_add_u32 s4, s10, s6
	v_lshl_add_u64 v[4:5], s[24:25], 0, v[2:3]
	v_and_b32_e32 v6, 0x60, v6
	v_mov_b32_e32 v7, v3
	v_lshlrev_b32_e32 v56, 4, v0
	v_mov_b32_e32 v57, v3
	s_addc_u32 s5, s11, s7
	v_lshl_add_u64 v[4:5], v[4:5], 0, v[6:7]
	s_movk_i32 s8, 0x2000
	v_lshl_add_u64 v[6:7], s[4:5], 0, v[56:57]
	global_load_dwordx4 v[8:11], v[4:5], off nt
	global_load_dwordx4 v[12:15], v[4:5], off offset:16 nt
	global_load_dwordx4 v[16:19], v56, s[4:5]
	v_add_co_u32_e64 v28, s[4:5], s8, v6
	s_mov_b32 s33, 0xa000
	s_nop 0
	v_addc_co_u32_e64 v29, s[4:5], 0, v7, s[4:5]
	s_movk_i32 s4, 0x4000
	s_nop 0
	v_add_co_u32_e64 v30, s[4:5], s4, v6
	s_mov_b32 s6, 0xe000
	s_nop 0
	v_addc_co_u32_e64 v31, s[4:5], 0, v7, s[4:5]
	global_load_dwordx4 v[20:23], v[28:29], off
	global_load_dwordx4 v[24:27], v[30:31], off
	s_movk_i32 s4, 0x6000
	v_add_co_u32_e64 v40, s[4:5], s4, v6
	v_lshlrev_b32_e32 v57, 6, v1
	s_nop 0
	v_addc_co_u32_e64 v41, s[4:5], 0, v7, s[4:5]
	global_load_dwordx4 v[28:31], v[40:41], off
	global_load_dwordx4 v[32:35], v[4:5], off offset:128 nt
	global_load_dwordx4 v[36:39], v[4:5], off offset:144 nt
	s_mov_b32 s4, 0x8000
	v_add_co_u32_e64 v40, s[4:5], s4, v6
	v_bitop3_b32 v58, v56, 48, v0 bitop3:0x48
	s_nop 0
	v_addc_co_u32_e64 v41, s[4:5], 0, v7, s[4:5]
	v_add_co_u32_e64 v44, s[4:5], s33, v6
	global_load_dwordx4 v[40:43], v[40:41], off
	s_nop 0
	v_addc_co_u32_e64 v45, s[4:5], 0, v7, s[4:5]
	s_mov_b32 s4, 0xc000
	s_nop 0
	v_add_co_u32_e64 v48, s[4:5], s4, v6
	global_load_dwordx4 v[44:47], v[44:45], off
	s_nop 0
	v_addc_co_u32_e64 v49, s[4:5], 0, v7, s[4:5]
	v_add_co_u32_e64 v52, s[4:5], s6, v6
	global_load_dwordx4 v[48:51], v[48:49], off
	s_nop 0
	v_addc_co_u32_e64 v53, s[4:5], 0, v7, s[4:5]
	global_load_dwordx4 v[52:55], v[52:53], off
	s_mov_b32 s4, 0x1e000
	v_add3_u32 v209, 0, v57, v58
	v_add_u32_e32 v208, 0, v56
	v_readfirstlane_b32 s30, v0
	v_bfe_u32 v207, v0, 5, 1
	v_bitop3_b32 v1, v207, v1, 3 bitop3:0x78
	v_lshlrev_b32_e32 v210, 4, v1
	s_mov_b32 s34, 0x14000
	v_add_u32_e32 v213, 0x2000, v208
	s_mov_b32 s43, 0
	s_lshr_b32 s29, s30, 6
	s_mov_b32 s35, -2
	s_mov_b32 s36, 0xffff2000
	s_mov_b32 s37, 0xffff4000
	s_mov_b32 s38, 0xffff6000
	s_movk_i32 s39, 0x8000
	s_movk_i32 s40, 0xa000
	s_movk_i32 s41, 0xc000
	s_movk_i32 s42, 0xe000
	s_mov_b64 s[26:27], 0x100
	v_mov_b32_e32 v56, v3
	v_mov_b32_e32 v57, v3
	v_mov_b32_e32 v58, v3
	v_mov_b32_e32 v59, v3
	v_mov_b32_e32 v60, v3
	v_mov_b32_e32 v61, v3
	v_mov_b32_e32 v62, v3
	v_mov_b32_e32 v63, v3
	v_mov_b32_e32 v64, v3
	v_mov_b32_e32 v65, v3
	v_mov_b32_e32 v66, v3
	v_mov_b32_e32 v67, v3
	v_mov_b32_e32 v68, v3
	v_mov_b32_e32 v69, v3
	v_mov_b32_e32 v70, v3
	s_waitcnt vmcnt(11)
	v_cvt_pk_f16_f32 v8, v8, v9
	v_cvt_pk_f16_f32 v9, v10, v11
	s_waitcnt vmcnt(10)
	v_cvt_pk_f16_f32 v10, v12, v13
	v_cvt_pk_f16_f32 v11, v14, v15
	ds_write_b128 v209, v[8:11]
	v_and_b32_e32 v10, 31, v0
	s_waitcnt vmcnt(9)
	ds_write_b128 v208, v[16:19] offset:8192
	s_waitcnt vmcnt(8)
	ds_write_b128 v208, v[20:23] offset:16384
	s_waitcnt vmcnt(7)
	ds_write_b128 v208, v[24:27] offset:24576
	s_load_dwordx2 s[16:17], s[0:1], 0x50
	s_load_dwordx4 s[12:15], s[0:1], 0x40
	s_load_dwordx8 s[4:11], s[0:1], 0x20
	s_lshl_b32 s0, s30, 1
	s_and_b32 s31, s0, 0x180
	s_lshr_b32 s0, s30, 2
	v_bfe_u32 v11, v0, 2, 2
	s_and_b32 s0, s0, 0x3fffffc0
	s_waitcnt vmcnt(5)
	v_cvt_pk_f16_f32 v8, v32, v33
	v_cvt_pk_f16_f32 v9, v34, v35
	v_or_b32_e32 v12, s31, v10
	v_or_b32_e32 v206, s0, v10
	v_bitop3_b32 v1, v207, v11, 2 bitop3:0x36
	s_waitcnt vmcnt(4)
	v_cvt_pk_f16_f32 v10, v36, v37
	v_cvt_pk_f16_f32 v11, v38, v39
	s_mov_b32 s0, 0x10000
	ds_write_b128 v208, v[28:31] offset:32768
	ds_write_b128 v209, v[8:11] offset:40960
	v_add_co_u32_e64 v8, s[0:1], s0, v6
	global_load_dwordx4 v[154:157], v[4:5], off offset:272 nt
	global_load_dwordx4 v[162:165], v[4:5], off offset:256 nt
	v_addc_co_u32_e64 v9, s[0:1], 0, v7, s[0:1]
	s_mov_b32 s0, 0x12000
	global_load_dwordx4 v[158:161], v[8:9], off
	v_add_co_u32_e64 v8, s[0:1], s0, v6
	v_lshl_add_u32 v211, v12, 6, 0
	s_nop 0
	v_addc_co_u32_e64 v9, s[0:1], 0, v7, s[0:1]
	v_add_co_u32_e64 v10, s[0:1], s34, v6
	v_add_u32_e32 v14, 0x12000, v208
	s_nop 0
	v_addc_co_u32_e64 v11, s[0:1], 0, v7, s[0:1]
	s_mov_b32 s0, 0x16000
	s_nop 0
	v_add_co_u32_e64 v12, s[0:1], s0, v6
	s_waitcnt vmcnt(3)
	ds_write_b128 v14, v[52:55]
	v_addc_co_u32_e64 v13, s[0:1], 0, v7, s[0:1]
	s_mov_b32 s0, 0x18000
	s_nop 0
	v_add_co_u32_e64 v14, s[0:1], s0, v6
	ds_write_b128 v208, v[40:43] offset:49152
	s_nop 0
	v_addc_co_u32_e64 v15, s[0:1], 0, v7, s[0:1]
	s_mov_b32 s0, 0x1a000
	s_nop 0
	v_add_co_u32_e64 v16, s[0:1], s0, v6
	ds_write_b128 v208, v[44:47] offset:57344
	s_nop 0
	v_addc_co_u32_e64 v17, s[0:1], 0, v7, s[0:1]
	s_mov_b32 s0, 0x1c000
	ds_write_b128 v213, v[48:51] offset:57344
	v_add_co_u32_e64 v18, s[0:1], s0, v6
	v_add_u32_e32 v216, v211, v210
	s_nop 0
	v_addc_co_u32_e64 v19, s[0:1], 0, v7, s[0:1]
	global_load_dwordx4 v[174:177], v[8:9], off
	global_load_dwordx4 v[166:169], v[10:11], off
	global_load_dwordx4 v[170:173], v[12:13], off
	global_load_dwordx4 v[142:145], v[4:5], off offset:400 nt
	global_load_dwordx4 v[150:153], v[4:5], off offset:384 nt
	global_load_dwordx4 v[138:141], v[14:15], off
	global_load_dwordx4 v[146:149], v[16:17], off
	global_load_dwordx4 v[134:137], v[18:19], off
	s_mov_b32 s0, 0x1e000
	v_add_co_u32_e64 v8, s[0:1], s0, v6
	s_nop 1
	v_addc_co_u32_e64 v9, s[0:1], 0, v7, s[0:1]
	global_load_dwordx4 v[130:133], v[8:9], off
	s_waitcnt lgkmcnt(0)
	s_barrier
	v_lshl_add_u32 v218, v206, 6, 0
	v_add_u32_e32 v217, v218, v210
	ds_read_b128 v[198:201], v216 offset:8192
	ds_read_b128 v[194:197], v216 offset:10240
	ds_read_b128 v[190:193], v216 offset:12288
	ds_read_b128 v[178:181], v216 offset:14336
	ds_read_b128 v[186:189], v217
	ds_read_b128 v[182:185], v217 offset:2048
	v_and_b32_e32 v20, 3, v0
	v_lshl_or_b32 v2, v20, 5, v2
	s_mov_b64 s[0:1], 0x2e000
	v_lshlrev_b32_e32 v212, 4, v1
	v_lshl_add_u64 v[202:203], v[6:7], 0, s[0:1]
	s_mov_b64 s[0:1], 0x290
	v_lshl_add_u64 v[4:5], s[24:25], 0, v[2:3]
	v_lshl_add_u64 v[204:205], v[4:5], 0, s[0:1]
	s_mov_b64 s[24:25], 0x10000
	v_mov_b32_e32 v2, v3
	v_mov_b32_e32 v4, v3
	v_mov_b32_e32 v5, v3
	v_mov_b32_e32 v6, v3
	v_mov_b32_e32 v7, v3
	v_mov_b32_e32 v8, v3
	v_mov_b32_e32 v9, v3
	v_mov_b32_e32 v10, v3
	v_mov_b32_e32 v11, v3
	v_mov_b32_e32 v12, v3
	v_mov_b32_e32 v13, v3
	v_mov_b32_e32 v14, v3
	v_mov_b32_e32 v15, v3
	v_mov_b32_e32 v16, v3
	v_mov_b32_e32 v17, v3
	v_mov_b32_e32 v18, v3
	v_mov_b32_e32 v19, v3
	v_mov_b32_e32 v20, v3
	v_mov_b32_e32 v21, v3
	v_mov_b32_e32 v22, v3
	v_mov_b32_e32 v23, v3
	v_mov_b32_e32 v24, v3
	v_mov_b32_e32 v25, v3
	v_mov_b32_e32 v26, v3
	v_mov_b32_e32 v27, v3
	v_mov_b32_e32 v28, v3
	v_mov_b32_e32 v29, v3
	v_mov_b32_e32 v30, v3
	v_mov_b32_e32 v31, v3
	v_mov_b32_e32 v32, v3
	v_mov_b32_e32 v33, v3
	v_mov_b32_e32 v34, v3
	v_mov_b32_e32 v35, v3
	v_mov_b32_e32 v36, v3
	v_mov_b32_e32 v37, v3
	v_mov_b32_e32 v38, v3
	v_mov_b32_e32 v39, v3
	v_mov_b32_e32 v40, v3
	v_mov_b32_e32 v41, v3
	v_mov_b32_e32 v42, v3
	v_mov_b32_e32 v43, v3
	v_mov_b32_e32 v44, v3
	v_mov_b32_e32 v45, v3
	v_mov_b32_e32 v46, v3
	v_mov_b32_e32 v47, v3
	v_mov_b32_e32 v48, v3
	v_mov_b32_e32 v49, v3
	v_mov_b32_e32 v50, v3
	v_mov_b32_e32 v51, v3
	v_mov_b32_e32 v52, v3
	v_mov_b32_e32 v53, v3
	v_mov_b32_e32 v54, v3
	v_mov_b32_e32 v55, v3
	v_mov_b32_e32 v71, v3
	v_mov_b32_e32 v72, v3
	v_mov_b32_e32 v73, v3
	v_mov_b32_e32 v74, v3
	v_mov_b32_e32 v75, v3
	v_mov_b32_e32 v76, v3
	v_mov_b32_e32 v77, v3
	v_mov_b32_e32 v78, v3
	v_mov_b32_e32 v79, v3
	v_mov_b32_e32 v80, v3
	v_mov_b32_e32 v81, v3
	v_mov_b32_e32 v82, v3
	v_mov_b32_e32 v83, v3
	v_mov_b32_e32 v84, v3
	v_mov_b32_e32 v85, v3
	v_mov_b32_e32 v86, v3
	v_mov_b32_e32 v87, v3
	v_mov_b32_e32 v88, v3
	v_mov_b32_e32 v89, v3
	v_mov_b32_e32 v90, v3
	v_mov_b32_e32 v91, v3
	v_mov_b32_e32 v92, v3
	v_mov_b32_e32 v93, v3
	v_mov_b32_e32 v94, v3
	v_mov_b32_e32 v95, v3
	v_mov_b32_e32 v96, v3
	v_mov_b32_e32 v97, v3
	v_mov_b32_e32 v98, v3
	v_mov_b32_e32 v99, v3
	v_mov_b32_e32 v100, v3
	v_mov_b32_e32 v101, v3
	v_mov_b32_e32 v102, v3
	v_mov_b32_e32 v103, v3
	v_mov_b32_e32 v104, v3
	v_mov_b32_e32 v105, v3
	v_mov_b32_e32 v106, v3
	v_mov_b32_e32 v107, v3
	v_mov_b32_e32 v108, v3
	v_mov_b32_e32 v109, v3
	v_mov_b32_e32 v110, v3
	v_mov_b32_e32 v111, v3
	v_mov_b32_e32 v112, v3
	v_mov_b32_e32 v113, v3
	v_mov_b32_e32 v114, v3
	v_mov_b32_e32 v115, v3
	v_mov_b32_e32 v116, v3
	v_mov_b32_e32 v117, v3
	v_mov_b32_e32 v118, v3
	v_mov_b32_e32 v119, v3
	v_mov_b32_e32 v120, v3
	v_mov_b32_e32 v121, v3
	v_mov_b32_e32 v122, v3
	v_mov_b32_e32 v123, v3
	v_mov_b32_e32 v124, v3
	v_mov_b32_e32 v125, v3
	v_mov_b32_e32 v126, v3
	v_mov_b32_e32 v127, v3
	v_mov_b32_e32 v128, v3
	v_mov_b32_e32 v129, v3
	v_and_b32_e32 v1, 63, v0
	v_add_u32_e32 v215, v211, v212
	v_add_u32_e32 v214, v218, v212
.LBB1_1:
	s_waitcnt lgkmcnt(0)
	v_mfma_f32_32x32x16_f16 v[114:129], v[198:201], v[186:189], v[114:129]
	s_mov_b32 s44, s33
	s_mov_b32 s33, s43
	v_mfma_f32_32x32x16_f16 v[98:113], v[198:201], v[182:185], v[98:113]
	v_add_u32_e32 v219, s33, v215
	ds_read_b128 v[198:201], v219 offset:8192
	ds_read_b128 v[220:223], v219 offset:10240
	ds_read_b128 v[224:227], v219 offset:12288
	ds_read_b128 v[228:231], v219 offset:14336
	v_add_u32_e32 v219, s33, v214
	ds_read_b128 v[232:235], v219
	ds_read_b128 v[236:239], v219 offset:2048
	s_waitcnt vmcnt(10)
	v_cvt_pk_f16_f32 v162, v162, v163
	v_cvt_pk_f16_f32 v163, v164, v165
	v_cvt_pk_f16_f32 v164, v154, v155
	v_cvt_pk_f16_f32 v165, v156, v157
	v_add_u32_e32 v154, s34, v209
	ds_write_b128 v154, v[162:165]
	v_mfma_f32_32x32x16_f16 v[82:97], v[194:197], v[186:189], v[82:97]
	v_add_u32_e32 v154, s34, v208
	s_waitcnt vmcnt(9)
	ds_write_b128 v154, v[158:161] offset:8192
	s_waitcnt vmcnt(8)
	ds_write_b128 v154, v[174:177] offset:16384
	v_mfma_f32_32x32x16_f16 v[66:81], v[194:197], v[182:185], v[66:81]
	v_mfma_f32_32x32x16_f16 v[50:65], v[190:193], v[186:189], v[50:65]
	s_waitcnt vmcnt(7)
	ds_write_b128 v154, v[166:169] offset:24576
	s_waitcnt vmcnt(6)
	ds_write_b128 v154, v[170:173] offset:32768
	v_mfma_f32_32x32x16_f16 v[34:49], v[190:193], v[182:185], v[34:49]
	v_add_co_u32_e64 v158, s[0:1], s36, v202
	global_load_dwordx4 v[154:157], v[204:205], off offset:-128 nt
	global_load_dwordx4 v[162:165], v[204:205], off offset:-144 nt
	v_addc_co_u32_e64 v159, s[0:1], -1, v203, s[0:1]
	v_add_co_u32_e64 v166, s[0:1], s37, v202
	v_mfma_f32_32x32x16_f16 v[18:33], v[178:181], v[186:189], v[18:33]
	s_nop 0
	v_addc_co_u32_e64 v167, s[0:1], -1, v203, s[0:1]
	global_load_dwordx4 v[158:161], v[158:159], off
	s_nop 0
	global_load_dwordx4 v[174:177], v[166:167], off
	v_add_co_u32_e64 v166, s[0:1], s38, v202
	s_nop 1
	v_addc_co_u32_e64 v167, s[0:1], -1, v203, s[0:1]
	v_add_co_u32_e64 v170, s[0:1], s39, v202
	v_mfma_f32_32x32x16_f16 v[2:17], v[178:181], v[182:185], v[2:17]
	s_nop 0
	v_addc_co_u32_e64 v171, s[0:1], -1, v203, s[0:1]
	global_load_dwordx4 v[166:169], v[166:167], off
	s_nop 0
	global_load_dwordx4 v[170:173], v[170:171], off
	v_add_u32_e32 v190, s44, v216
	ds_read_b128 v[178:181], v190 offset:8192
	ds_read_b128 v[182:185], v190 offset:10240
	ds_read_b128 v[186:189], v190 offset:12288
	ds_read_b128 v[190:193], v190 offset:14336
	v_add_u32_e32 v219, s44, v217
	ds_read_b128 v[194:197], v219
	ds_read_b128 v[240:243], v219 offset:2048
	s_waitcnt lgkmcnt(12)
	v_mfma_f32_32x32x16_f16 v[114:129], v[198:201], v[232:235], v[114:129]
	s_waitcnt lgkmcnt(11)
	v_mfma_f32_32x32x16_f16 v[98:113], v[198:201], v[236:239], v[98:113]
	v_mfma_f32_32x32x16_f16 v[82:97], v[220:223], v[232:235], v[82:97]
	v_mfma_f32_32x32x16_f16 v[66:81], v[220:223], v[236:239], v[66:81]
	v_mfma_f32_32x32x16_f16 v[50:65], v[224:227], v[232:235], v[50:65]
	v_mfma_f32_32x32x16_f16 v[34:49], v[224:227], v[236:239], v[34:49]
	v_mfma_f32_32x32x16_f16 v[18:33], v[228:231], v[232:235], v[18:33]
	v_mfma_f32_32x32x16_f16 v[2:17], v[228:231], v[236:239], v[2:17]
	s_waitcnt lgkmcnt(1)
	v_mfma_f32_32x32x16_f16 v[114:129], v[178:181], v[194:197], v[114:129]
	s_waitcnt lgkmcnt(0)
	s_barrier
	s_waitcnt lgkmcnt(0)
	v_mfma_f32_32x32x16_f16 v[98:113], v[178:181], v[240:243], v[98:113]
	v_add_u32_e32 v178, s44, v215
	ds_read_b128 v[220:223], v178 offset:8192
	ds_read_b128 v[224:227], v178 offset:10240
	ds_read_b128 v[228:231], v178 offset:12288
	ds_read_b128 v[232:235], v178 offset:14336
	v_add_u32_e32 v178, s44, v214
	ds_read_b128 v[236:239], v178
	ds_read_b128 v[244:247], v178 offset:2048
	s_waitcnt vmcnt(10)
	v_cvt_pk_f16_f32 v150, v150, v151
	v_cvt_pk_f16_f32 v151, v152, v153
	v_cvt_pk_f16_f32 v152, v142, v143
	v_cvt_pk_f16_f32 v153, v144, v145
	v_add_u32_e32 v142, s33, v209
	ds_write_b128 v142, v[150:153]
	v_mfma_f32_32x32x16_f16 v[82:97], v[182:185], v[194:197], v[82:97]
	v_add_u32_e32 v142, s33, v208
	s_waitcnt vmcnt(9)
	ds_write_b128 v142, v[138:141] offset:8192
	s_waitcnt vmcnt(8)
	ds_write_b128 v142, v[146:149] offset:16384
	v_mfma_f32_32x32x16_f16 v[66:81], v[182:185], v[240:243], v[66:81]
	v_mfma_f32_32x32x16_f16 v[50:65], v[186:189], v[194:197], v[50:65]
	s_waitcnt vmcnt(7)
	ds_write_b128 v142, v[134:137] offset:24576
	s_waitcnt vmcnt(6)
	ds_write_b128 v142, v[130:133] offset:32768
	v_mfma_f32_32x32x16_f16 v[34:49], v[186:189], v[240:243], v[34:49]
	v_add_co_u32_e64 v130, s[0:1], s40, v202
	global_load_dwordx4 v[142:145], v[204:205], off nt
	global_load_dwordx4 v[150:153], v[204:205], off offset:-16 nt
	v_addc_co_u32_e64 v131, s[0:1], -1, v203, s[0:1]
	v_add_co_u32_e64 v132, s[0:1], s41, v202
	v_mfma_f32_32x32x16_f16 v[18:33], v[190:193], v[194:197], v[18:33]
	s_nop 0
	v_addc_co_u32_e64 v133, s[0:1], -1, v203, s[0:1]
	global_load_dwordx4 v[138:141], v[130:131], off
	global_load_dwordx4 v[146:149], v[132:133], off
	v_add_co_u32_e64 v130, s[0:1], s42, v202
	s_nop 1
	v_addc_co_u32_e64 v131, s[0:1], -1, v203, s[0:1]
	global_load_dwordx4 v[134:137], v[130:131], off
	s_nop 0
	global_load_dwordx4 v[130:133], v[202:203], off
	v_mfma_f32_32x32x16_f16 v[2:17], v[190:193], v[240:243], v[2:17]
	v_add_u32_e32 v178, s34, v216
	ds_read_b128 v[198:201], v178 offset:8192
	ds_read_b128 v[194:197], v178 offset:10240
	ds_read_b128 v[190:193], v178 offset:12288
	ds_read_b128 v[178:181], v178 offset:14336
	v_add_u32_e32 v182, s34, v217
	ds_read_b128 v[186:189], v182
	ds_read_b128 v[182:185], v182 offset:2048
	s_waitcnt lgkmcnt(12)
	v_mfma_f32_32x32x16_f16 v[114:129], v[220:223], v[236:239], v[114:129]
	s_waitcnt lgkmcnt(11)
	v_mfma_f32_32x32x16_f16 v[98:113], v[220:223], v[244:247], v[98:113]
	v_mfma_f32_32x32x16_f16 v[82:97], v[224:227], v[236:239], v[82:97]
	v_mfma_f32_32x32x16_f16 v[66:81], v[224:227], v[244:247], v[66:81]
	v_mfma_f32_32x32x16_f16 v[50:65], v[228:231], v[236:239], v[50:65]
	v_mfma_f32_32x32x16_f16 v[34:49], v[228:231], v[244:247], v[34:49]
	v_mfma_f32_32x32x16_f16 v[18:33], v[232:235], v[236:239], v[18:33]
	v_mfma_f32_32x32x16_f16 v[2:17], v[232:235], v[244:247], v[2:17]
	s_waitcnt lgkmcnt(0)
	s_barrier
	s_add_i32 s35, s35, 2
	v_lshl_add_u64 v[202:203], v[202:203], 0, s[24:25]
	v_lshl_add_u64 v[204:205], v[204:205], 0, s[26:27]
	s_mov_b32 s43, s34
	s_cmp_gt_u32 s35, 9
	s_mov_b32 s34, s44
	s_cbranch_scc0 .LBB1_1
	s_and_b64 s[0:1], s[20:21], exec
	s_cselect_b32 s6, s6, s8
	s_cselect_b32 s7, s7, s9
	s_and_b64 s[0:1], vcc, exec
	s_cselect_b32 s1, s5, s7
	s_cselect_b32 s0, s4, s6
	v_mov_b32_e32 v202, 0x3e38aa3b
	s_waitcnt lgkmcnt(1)
	v_mfma_f32_32x32x16_f16 v[114:129], v[198:201], v[186:189], v[114:129]
	v_cndmask_b32_e32 v202, 1.0, v202, vcc
	s_waitcnt lgkmcnt(0)
	v_mfma_f32_32x32x16_f16 v[98:113], v[198:201], v[182:185], v[98:113]
	ds_read_b128 v[198:201], v215 offset:8192
	ds_read_b128 v[220:223], v215 offset:10240
	ds_read_b128 v[224:227], v215 offset:12288
	ds_read_b128 v[228:231], v215 offset:14336
	ds_read_b128 v[232:235], v214
	ds_read_b128 v[236:239], v214 offset:2048
	s_waitcnt vmcnt(10)
	v_cvt_pk_f16_f32 v162, v162, v163
	v_cvt_pk_f16_f32 v163, v164, v165
	v_cvt_pk_f16_f32 v164, v154, v155
	v_cvt_pk_f16_f32 v165, v156, v157
	v_add_u32_e32 v154, 0x14000, v209
	ds_write_b128 v154, v[162:165]
	v_add_u32_e32 v154, 0x14000, v213
	s_waitcnt vmcnt(9)
	ds_write_b128 v154, v[158:161]
	v_add_u32_e32 v154, 0x16000, v213
	v_mfma_f32_32x32x16_f16 v[82:97], v[194:197], v[186:189], v[82:97]
	s_waitcnt vmcnt(8)
	ds_write_b128 v154, v[174:177]
	v_mfma_f32_32x32x16_f16 v[66:81], v[194:197], v[182:185], v[66:81]
	v_add_u32_e32 v154, 0x18000, v213
	s_waitcnt vmcnt(7)
	ds_write_b128 v154, v[166:169]
	v_add_u32_e32 v154, 0x1a000, v213
	v_mfma_f32_32x32x16_f16 v[50:65], v[190:193], v[186:189], v[50:65]
	s_waitcnt vmcnt(6)
	ds_write_b128 v154, v[170:173]
	v_mfma_f32_32x32x16_f16 v[34:49], v[190:193], v[182:185], v[34:49]
	v_mfma_f32_32x32x16_f16 v[18:33], v[178:181], v[186:189], v[18:33]
	v_mfma_f32_32x32x16_f16 v[2:17], v[178:181], v[182:185], v[2:17]
	ds_read_b128 v[154:157], v216 offset:49152
	ds_read_b128 v[158:161], v216 offset:51200
	ds_read_b128 v[162:165], v216 offset:53248
	ds_read_b128 v[166:169], v216 offset:55296
	ds_read_b128 v[170:173], v217 offset:40960
	ds_read_b128 v[174:177], v217 offset:43008
	s_waitcnt lgkmcnt(12)
	v_mfma_f32_32x32x16_f16 v[114:129], v[198:201], v[232:235], v[114:129]
	s_waitcnt lgkmcnt(11)
	v_mfma_f32_32x32x16_f16 v[98:113], v[198:201], v[236:239], v[98:113]
	v_mfma_f32_32x32x16_f16 v[82:97], v[220:223], v[232:235], v[82:97]
	v_mfma_f32_32x32x16_f16 v[66:81], v[220:223], v[236:239], v[66:81]
	v_mfma_f32_32x32x16_f16 v[50:65], v[224:227], v[232:235], v[50:65]
	v_mfma_f32_32x32x16_f16 v[34:49], v[224:227], v[236:239], v[34:49]
	v_mfma_f32_32x32x16_f16 v[18:33], v[228:231], v[232:235], v[18:33]
	v_mfma_f32_32x32x16_f16 v[2:17], v[228:231], v[236:239], v[2:17]
	s_waitcnt lgkmcnt(0)
	s_barrier
	s_waitcnt lgkmcnt(1)
	v_mfma_f32_32x32x16_f16 v[114:129], v[154:157], v[170:173], v[114:129]
	s_waitcnt lgkmcnt(0)
	v_mfma_f32_32x32x16_f16 v[98:113], v[154:157], v[174:177], v[98:113]
	ds_read_b128 v[154:157], v215 offset:49152
	ds_read_b128 v[178:181], v215 offset:51200
	ds_read_b128 v[182:185], v215 offset:53248
	ds_read_b128 v[186:189], v215 offset:55296
	ds_read_b128 v[190:193], v214 offset:40960
	ds_read_b128 v[194:197], v214 offset:43008
	s_waitcnt vmcnt(4)
	v_cvt_pk_f16_f32 v150, v150, v151
	v_cvt_pk_f16_f32 v151, v152, v153
	v_cvt_pk_f16_f32 v152, v142, v143
	v_cvt_pk_f16_f32 v153, v144, v145
	ds_write_b128 v209, v[150:153]
	v_mfma_f32_32x32x16_f16 v[82:97], v[158:161], v[170:173], v[82:97]
	s_waitcnt vmcnt(3)
	ds_write_b128 v208, v[138:141] offset:8192
	s_waitcnt vmcnt(2)
	ds_write_b128 v208, v[146:149] offset:16384
	v_mfma_f32_32x32x16_f16 v[66:81], v[158:161], v[174:177], v[66:81]
	v_mfma_f32_32x32x16_f16 v[50:65], v[162:165], v[170:173], v[50:65]
	s_waitcnt vmcnt(1)
	ds_write_b128 v208, v[134:137] offset:24576
	s_waitcnt vmcnt(0)
	ds_write_b128 v208, v[130:133] offset:32768
	v_mfma_f32_32x32x16_f16 v[34:49], v[162:165], v[174:177], v[34:49]
	v_mfma_f32_32x32x16_f16 v[18:33], v[166:169], v[170:173], v[18:33]
	v_mfma_f32_32x32x16_f16 v[2:17], v[166:169], v[174:177], v[2:17]
	v_add_u32_e32 v158, 0x16000, v211
	v_add_u32_e32 v142, v158, v210
	ds_read_b128 v[130:133], v142
	ds_read_b128 v[134:137], v142 offset:2048
	ds_read_b128 v[138:141], v142 offset:4096
	ds_read_b128 v[142:145], v142 offset:6144
	v_add_u32_e32 v166, 0x14000, v218
	v_add_u32_e32 v150, v166, v210
	ds_read_b128 v[146:149], v150
	ds_read_b128 v[150:153], v150 offset:2048
	s_waitcnt lgkmcnt(12)
	v_mfma_f32_32x32x16_f16 v[114:129], v[154:157], v[190:193], v[114:129]
	s_waitcnt lgkmcnt(11)
	v_mfma_f32_32x32x16_f16 v[98:113], v[154:157], v[194:197], v[98:113]
	v_mfma_f32_32x32x16_f16 v[82:97], v[178:181], v[190:193], v[82:97]
	v_mfma_f32_32x32x16_f16 v[66:81], v[178:181], v[194:197], v[66:81]
	v_mfma_f32_32x32x16_f16 v[50:65], v[182:185], v[190:193], v[50:65]
	v_mfma_f32_32x32x16_f16 v[34:49], v[182:185], v[194:197], v[34:49]
	v_mfma_f32_32x32x16_f16 v[18:33], v[186:189], v[190:193], v[18:33]
	v_mfma_f32_32x32x16_f16 v[2:17], v[186:189], v[194:197], v[2:17]
	s_waitcnt lgkmcnt(0)
	s_barrier
	s_waitcnt lgkmcnt(1)
	v_mfma_f32_32x32x16_f16 v[114:129], v[130:133], v[146:149], v[114:129]
	s_waitcnt lgkmcnt(0)
	v_mfma_f32_32x32x16_f16 v[98:113], v[130:133], v[150:153], v[98:113]
	v_add_u32_e32 v162, v158, v212
	ds_read_b128 v[130:133], v162
	ds_read_b128 v[154:157], v162 offset:2048
	ds_read_b128 v[158:161], v162 offset:4096
	ds_read_b128 v[162:165], v162 offset:6144
	v_add_u32_e32 v170, v166, v212
	ds_read_b128 v[166:169], v170
	ds_read_b128 v[170:173], v170 offset:2048
	v_mfma_f32_32x32x16_f16 v[82:97], v[134:137], v[146:149], v[82:97]
	v_mfma_f32_32x32x16_f16 v[66:81], v[134:137], v[150:153], v[66:81]
	v_mfma_f32_32x32x16_f16 v[50:65], v[138:141], v[146:149], v[50:65]
	v_mfma_f32_32x32x16_f16 v[34:49], v[138:141], v[150:153], v[34:49]
	v_mfma_f32_32x32x16_f16 v[18:33], v[142:145], v[146:149], v[18:33]
	v_mfma_f32_32x32x16_f16 v[2:17], v[142:145], v[150:153], v[2:17]
	ds_read_b128 v[134:137], v216 offset:8192
	ds_read_b128 v[138:141], v216 offset:10240
	ds_read_b128 v[142:145], v216 offset:12288
	ds_read_b128 v[146:149], v216 offset:14336
	ds_read_b128 v[150:153], v217
	ds_read_b128 v[174:177], v217 offset:2048
	s_waitcnt lgkmcnt(7)
	v_mfma_f32_32x32x16_f16 v[114:129], v[130:133], v[166:169], v[114:129]
	s_waitcnt lgkmcnt(6)
	v_mfma_f32_32x32x16_f16 v[98:113], v[130:133], v[170:173], v[98:113]
	v_mfma_f32_32x32x16_f16 v[82:97], v[154:157], v[166:169], v[82:97]
	v_mfma_f32_32x32x16_f16 v[66:81], v[154:157], v[170:173], v[66:81]
	v_mfma_f32_32x32x16_f16 v[50:65], v[158:161], v[166:169], v[50:65]
	v_mfma_f32_32x32x16_f16 v[34:49], v[158:161], v[170:173], v[34:49]
	v_mfma_f32_32x32x16_f16 v[18:33], v[162:165], v[166:169], v[18:33]
	v_mfma_f32_32x32x16_f16 v[2:17], v[162:165], v[170:173], v[2:17]
	s_waitcnt lgkmcnt(0)
	s_barrier
	s_waitcnt lgkmcnt(1)
	v_mfma_f32_32x32x16_f16 v[114:129], v[134:137], v[150:153], v[114:129]
	s_waitcnt lgkmcnt(0)
	v_mfma_f32_32x32x16_f16 v[98:113], v[134:137], v[174:177], v[98:113]
	ds_read_b128 v[130:133], v215 offset:8192
	ds_read_b128 v[134:137], v215 offset:10240
	ds_read_b128 v[154:157], v215 offset:12288
	ds_read_b128 v[158:161], v215 offset:14336
	ds_read_b128 v[162:165], v214
	ds_read_b128 v[166:169], v214 offset:2048
	v_mfma_f32_32x32x16_f16 v[82:97], v[138:141], v[150:153], v[82:97]
	v_mfma_f32_32x32x16_f16 v[66:81], v[138:141], v[174:177], v[66:81]
	v_mfma_f32_32x32x16_f16 v[50:65], v[142:145], v[150:153], v[50:65]
	v_mfma_f32_32x32x16_f16 v[34:49], v[142:145], v[174:177], v[34:49]
	v_mfma_f32_32x32x16_f16 v[18:33], v[146:149], v[150:153], v[18:33]
	v_mfma_f32_32x32x16_f16 v[2:17], v[146:149], v[174:177], v[2:17]
	s_waitcnt lgkmcnt(1)
	v_mfma_f32_32x32x16_f16 v[114:129], v[130:133], v[162:165], v[114:129]
	s_waitcnt lgkmcnt(0)
	v_mfma_f32_32x32x16_f16 v[98:113], v[130:133], v[166:169], v[98:113]
	v_mfma_f32_32x32x16_f16 v[82:97], v[134:137], v[162:165], v[82:97]
	v_mfma_f32_32x32x16_f16 v[66:81], v[134:137], v[166:169], v[66:81]
	v_mfma_f32_32x32x16_f16 v[50:65], v[154:157], v[162:165], v[50:65]
	v_mfma_f32_32x32x16_f16 v[34:49], v[154:157], v[166:169], v[34:49]
	v_mfma_f32_32x32x16_f16 v[18:33], v[158:161], v[162:165], v[18:33]
	v_mfma_f32_32x32x16_f16 v[2:17], v[158:161], v[166:169], v[2:17]
	v_lshl_or_b32 v130, v207, 2, s31
	s_waitcnt lgkmcnt(0)
	s_barrier
	v_lshlrev_b32_e32 v154, 2, v130
	global_load_dwordx4 v[134:137], v154, s[0:1]
	global_load_dwordx4 v[150:153], v154, s[0:1] offset:32
	global_load_dwordx4 v[156:159], v154, s[0:1] offset:64
	global_load_dwordx4 v[160:163], v154, s[0:1] offset:96
	global_load_dwordx4 v[164:167], v154, s[0:1] offset:128
	global_load_dwordx4 v[168:171], v154, s[0:1] offset:160
	s_movk_i32 s4, 0x410
	v_lshlrev_b32_e32 v130, 1, v130
	v_mul_lo_u32 v131, v206, s4
	v_add3_u32 v155, 0, v130, v131
	global_load_dwordx4 v[172:175], v154, s[0:1] offset:192
	global_load_dwordx4 v[146:149], v154, s[0:1] offset:224
	global_load_dwordx4 v[142:145], v154, s[0:1] offset:256
	global_load_dwordx4 v[130:133], v154, s[0:1] offset:288
	global_load_dwordx4 v[138:141], v154, s[0:1] offset:320
	v_add_u32_e32 v176, 0x8000, v155
	s_waitcnt vmcnt(10)
	v_pk_add_f32 v[114:115], v[134:135], v[114:115]
	v_pk_add_f32 v[116:117], v[136:137], v[116:117]
	v_pk_add_f32 v[98:99], v[134:135], v[98:99]
	v_pk_add_f32 v[100:101], v[136:137], v[100:101]
	s_waitcnt vmcnt(9)
	v_pk_add_f32 v[118:119], v[150:151], v[118:119]
	v_pk_add_f32 v[120:121], v[152:153], v[120:121]
	s_waitcnt vmcnt(6)
	v_pk_add_f32 v[82:83], v[164:165], v[82:83]
	v_pk_add_f32 v[84:85], v[166:167], v[84:85]
	v_pk_add_f32 v[66:67], v[164:165], v[66:67]
	v_pk_add_f32 v[68:69], v[166:167], v[68:69]
	s_waitcnt vmcnt(5)
	v_pk_add_f32 v[70:71], v[168:169], v[70:71]
	v_pk_add_f32 v[72:73], v[170:171], v[72:73]
	v_pk_add_f32 v[102:103], v[150:151], v[102:103]
	v_pk_add_f32 v[104:105], v[152:153], v[104:105]
	v_pk_add_f32 v[122:123], v[156:157], v[122:123]
	v_pk_add_f32 v[124:125], v[158:159], v[124:125]
	v_pk_add_f32 v[106:107], v[156:157], v[106:107]
	v_pk_add_f32 v[108:109], v[158:159], v[108:109]
	v_pk_add_f32 v[126:127], v[160:161], v[126:127]
	v_pk_add_f32 v[128:129], v[162:163], v[128:129]
	v_pk_add_f32 v[110:111], v[160:161], v[110:111]
	v_pk_add_f32 v[112:113], v[162:163], v[112:113]
	v_pk_add_f32 v[86:87], v[168:169], v[86:87]
	v_pk_mul_f32 v[114:115], v[202:203], v[114:115] op_sel_hi:[0,1]
	v_pk_mul_f32 v[116:117], v[202:203], v[116:117] op_sel_hi:[0,1]
	v_pk_mul_f32 v[98:99], v[202:203], v[98:99] op_sel_hi:[0,1]
	v_pk_mul_f32 v[100:101], v[202:203], v[100:101] op_sel_hi:[0,1]
	v_pk_mul_f32 v[118:119], v[202:203], v[118:119] op_sel_hi:[0,1]
	v_pk_mul_f32 v[120:121], v[202:203], v[120:121] op_sel_hi:[0,1]
	v_pk_mul_f32 v[82:83], v[202:203], v[82:83] op_sel_hi:[0,1]
	v_pk_mul_f32 v[84:85], v[202:203], v[84:85] op_sel_hi:[0,1]
	v_pk_mul_f32 v[66:67], v[202:203], v[66:67] op_sel_hi:[0,1]
	v_pk_mul_f32 v[68:69], v[202:203], v[68:69] op_sel_hi:[0,1]
	v_pk_add_f32 v[88:89], v[170:171], v[88:89]
	v_pk_mul_f32 v[70:71], v[202:203], v[70:71] op_sel_hi:[0,1]
	v_pk_mul_f32 v[72:73], v[202:203], v[72:73] op_sel_hi:[0,1]
	v_pk_mul_f32 v[102:103], v[202:203], v[102:103] op_sel_hi:[0,1]
	v_pk_mul_f32 v[104:105], v[202:203], v[104:105] op_sel_hi:[0,1]
	v_pk_mul_f32 v[122:123], v[202:203], v[122:123] op_sel_hi:[0,1]
	v_pk_mul_f32 v[124:125], v[202:203], v[124:125] op_sel_hi:[0,1]
	v_pk_mul_f32 v[106:107], v[202:203], v[106:107] op_sel_hi:[0,1]
	v_pk_mul_f32 v[108:109], v[202:203], v[108:109] op_sel_hi:[0,1]
	v_pk_mul_f32 v[126:127], v[202:203], v[126:127] op_sel_hi:[0,1]
	v_pk_mul_f32 v[128:129], v[202:203], v[128:129] op_sel_hi:[0,1]
	v_pk_mul_f32 v[110:111], v[202:203], v[110:111] op_sel_hi:[0,1]
	v_pk_mul_f32 v[112:113], v[202:203], v[112:113] op_sel_hi:[0,1]
	v_pk_mul_f32 v[86:87], v[202:203], v[86:87] op_sel_hi:[0,1]
	v_cvt_pk_f16_f32 v114, v114, v115
	v_cvt_pk_f16_f32 v115, v116, v117
	v_cvt_pk_f16_f32 v98, v98, v99
	v_cvt_pk_f16_f32 v99, v100, v101
	v_cvt_pk_f16_f32 v100, v118, v119
	v_cvt_pk_f16_f32 v101, v120, v121
	v_cvt_pk_f16_f32 v82, v82, v83
	v_cvt_pk_f16_f32 v83, v84, v85
	v_cvt_pk_f16_f32 v84, v66, v67
	v_cvt_pk_f16_f32 v85, v68, v69
	v_pk_mul_f32 v[88:89], v[202:203], v[88:89] op_sel_hi:[0,1]
	v_cvt_pk_f16_f32 v70, v70, v71
	v_cvt_pk_f16_f32 v71, v72, v73
	v_cvt_pk_f16_f32 v102, v102, v103
	v_cvt_pk_f16_f32 v103, v104, v105
	v_cvt_pk_f16_f32 v104, v122, v123
	v_cvt_pk_f16_f32 v105, v124, v125
	v_cvt_pk_f16_f32 v106, v106, v107
	v_cvt_pk_f16_f32 v107, v108, v109
	v_cvt_pk_f16_f32 v108, v126, v127
	v_cvt_pk_f16_f32 v109, v128, v129
	v_cvt_pk_f16_f32 v110, v110, v111
	v_cvt_pk_f16_f32 v111, v112, v113
	v_cvt_pk_f16_f32 v86, v86, v87
	ds_write2_b64 v155, v[114:115], v[100:101] offset1:2
	ds_write2_b64 v176, v[98:99], v[102:103] offset0:64 offset1:66
	ds_write2_b64 v155, v[104:105], v[108:109] offset0:4 offset1:6
	ds_write2_b64 v176, v[106:107], v[110:111] offset0:68 offset1:70
	v_cvt_pk_f16_f32 v87, v88, v89
	ds_write2_b64 v176, v[84:85], v[70:71] offset0:72 offset1:74
	s_waitcnt vmcnt(4)
	v_pk_add_f32 v[70:71], v[172:173], v[90:91]
	v_pk_add_f32 v[84:85], v[174:175], v[92:93]
	v_pk_add_f32 v[74:75], v[172:173], v[74:75]
	ds_write2_b64 v155, v[82:83], v[86:87] offset0:8 offset1:10
	v_pk_mul_f32 v[82:83], v[202:203], v[70:71] op_sel_hi:[0,1]
	v_pk_mul_f32 v[84:85], v[202:203], v[84:85] op_sel_hi:[0,1]
	v_pk_mul_f32 v[74:75], v[202:203], v[74:75] op_sel_hi:[0,1]
	global_load_dwordx4 v[66:69], v154, s[0:1] offset:352
	global_load_dwordx4 v[70:73], v154, s[0:1] offset:384
	v_cvt_pk_f16_f32 v82, v82, v83
	v_cvt_pk_f16_f32 v83, v84, v85
	v_cvt_pk_f16_f32 v84, v74, v75
	v_pk_add_f32 v[74:75], v[174:175], v[76:77]
	s_waitcnt vmcnt(5)
	v_pk_add_f32 v[78:79], v[146:147], v[78:79]
	v_pk_mul_f32 v[74:75], v[202:203], v[74:75] op_sel_hi:[0,1]
	v_cvt_pk_f16_f32 v85, v74, v75
	global_load_dwordx4 v[74:77], v154, s[0:1] offset:416
	v_pk_add_f32 v[80:81], v[148:149], v[80:81]
	v_pk_mul_f32 v[78:79], v[202:203], v[78:79] op_sel_hi:[0,1]
	v_pk_mul_f32 v[80:81], v[202:203], v[80:81] op_sel_hi:[0,1]
	v_cvt_pk_f16_f32 v78, v78, v79
	v_cvt_pk_f16_f32 v79, v80, v81
	ds_write2_b64 v176, v[84:85], v[78:79] offset0:76 offset1:78
	global_load_dwordx4 v[78:81], v154, s[0:1] offset:448
	v_pk_add_f32 v[86:87], v[146:147], v[94:95]
	v_pk_add_f32 v[88:89], v[148:149], v[96:97]
	s_waitcnt vmcnt(6)
	v_pk_add_f32 v[50:51], v[142:143], v[50:51]
	v_pk_add_f32 v[52:53], v[144:145], v[52:53]
	v_pk_add_f32 v[34:35], v[142:143], v[34:35]
	v_pk_mul_f32 v[86:87], v[202:203], v[86:87] op_sel_hi:[0,1]
	v_pk_mul_f32 v[88:89], v[202:203], v[88:89] op_sel_hi:[0,1]
	v_pk_mul_f32 v[50:51], v[202:203], v[50:51] op_sel_hi:[0,1]
	v_pk_mul_f32 v[52:53], v[202:203], v[52:53] op_sel_hi:[0,1]
	v_pk_mul_f32 v[34:35], v[202:203], v[34:35] op_sel_hi:[0,1]
	v_cvt_pk_f16_f32 v86, v86, v87
	v_cvt_pk_f16_f32 v87, v88, v89
	v_cvt_pk_f16_f32 v50, v50, v51
	v_cvt_pk_f16_f32 v51, v52, v53
	v_cvt_pk_f16_f32 v52, v34, v35
	v_pk_add_f32 v[34:35], v[144:145], v[36:37]
	ds_write2_b64 v155, v[82:83], v[86:87] offset0:12 offset1:14
	v_pk_mul_f32 v[82:83], v[202:203], v[34:35] op_sel_hi:[0,1]
	global_load_dwordx4 v[34:37], v154, s[0:1] offset:480
	s_waitcnt vmcnt(6)
	v_pk_add_f32 v[38:39], v[130:131], v[38:39]
	v_pk_add_f32 v[40:41], v[132:133], v[40:41]
	v_pk_mul_f32 v[38:39], v[202:203], v[38:39] op_sel_hi:[0,1]
	v_pk_mul_f32 v[40:41], v[202:203], v[40:41] op_sel_hi:[0,1]
	v_cvt_pk_f16_f32 v53, v82, v83
	v_cvt_pk_f16_f32 v38, v38, v39
	v_cvt_pk_f16_f32 v39, v40, v41
	ds_write2_b64 v176, v[52:53], v[38:39] offset0:80 offset1:82
	s_waitcnt vmcnt(5)
	v_pk_add_f32 v[38:39], v[138:139], v[58:59]
	v_pk_add_f32 v[40:41], v[140:141], v[60:61]
	v_pk_mul_f32 v[38:39], v[202:203], v[38:39] op_sel_hi:[0,1]
	v_pk_mul_f32 v[40:41], v[202:203], v[40:41] op_sel_hi:[0,1]
	v_cvt_pk_f16_f32 v38, v38, v39
	v_cvt_pk_f16_f32 v39, v40, v41
	v_pk_add_f32 v[40:41], v[138:139], v[42:43]
	v_pk_add_f32 v[42:43], v[140:141], v[44:45]
	v_pk_mul_f32 v[40:41], v[202:203], v[40:41] op_sel_hi:[0,1]
	v_pk_mul_f32 v[42:43], v[202:203], v[42:43] op_sel_hi:[0,1]
	v_cvt_pk_f16_f32 v40, v40, v41
	v_cvt_pk_f16_f32 v41, v42, v43
	v_pk_add_f32 v[54:55], v[130:131], v[54:55]
	v_pk_add_f32 v[56:57], v[132:133], v[56:57]
	v_pk_mul_f32 v[54:55], v[202:203], v[54:55] op_sel_hi:[0,1]
	v_pk_mul_f32 v[56:57], v[202:203], v[56:57] op_sel_hi:[0,1]
	v_cmp_gt_u32_e64 s[0:1], 8, v0
	v_cvt_pk_f16_f32 v54, v54, v55
	v_cvt_pk_f16_f32 v55, v56, v57
	s_and_b64 s[6:7], s[20:21], s[0:1]
	ds_write2_b64 v155, v[50:51], v[54:55] offset0:16 offset1:18
	s_waitcnt vmcnt(4)
	v_pk_add_f32 v[42:43], v[66:67], v[62:63]
	s_waitcnt vmcnt(3)
	v_pk_add_f32 v[18:19], v[70:71], v[18:19]
	v_pk_add_f32 v[20:21], v[72:73], v[20:21]
	v_pk_add_f32 v[2:3], v[70:71], v[2:3]
	v_pk_add_f32 v[4:5], v[72:73], v[4:5]
	v_pk_mul_f32 v[18:19], v[202:203], v[18:19] op_sel_hi:[0,1]
	v_pk_mul_f32 v[20:21], v[202:203], v[20:21] op_sel_hi:[0,1]
	v_pk_mul_f32 v[2:3], v[202:203], v[2:3] op_sel_hi:[0,1]
	v_pk_mul_f32 v[4:5], v[202:203], v[4:5] op_sel_hi:[0,1]
	v_cvt_pk_f16_f32 v18, v18, v19
	v_cvt_pk_f16_f32 v19, v20, v21
	v_cvt_pk_f16_f32 v2, v2, v3
	v_cvt_pk_f16_f32 v3, v4, v5
	s_waitcnt vmcnt(2)
	v_pk_add_f32 v[4:5], v[74:75], v[22:23]
	v_pk_add_f32 v[20:21], v[76:77], v[24:25]
	v_pk_mul_f32 v[4:5], v[202:203], v[4:5] op_sel_hi:[0,1]
	v_pk_mul_f32 v[20:21], v[202:203], v[20:21] op_sel_hi:[0,1]
	v_cvt_pk_f16_f32 v4, v4, v5
	v_cvt_pk_f16_f32 v5, v20, v21
	ds_write2_b64 v155, v[18:19], v[4:5] offset0:24 offset1:26
	v_pk_add_f32 v[4:5], v[74:75], v[6:7]
	v_pk_add_f32 v[6:7], v[76:77], v[8:9]
	v_pk_mul_f32 v[4:5], v[202:203], v[4:5] op_sel_hi:[0,1]
	v_pk_mul_f32 v[6:7], v[202:203], v[6:7] op_sel_hi:[0,1]
	v_cvt_pk_f16_f32 v4, v4, v5
	v_cvt_pk_f16_f32 v5, v6, v7
	ds_write2_b64 v176, v[2:3], v[4:5] offset0:88 offset1:90
	s_waitcnt vmcnt(1)
	v_pk_add_f32 v[2:3], v[78:79], v[26:27]
	v_pk_add_f32 v[4:5], v[80:81], v[28:29]
	v_pk_mul_f32 v[2:3], v[202:203], v[2:3] op_sel_hi:[0,1]
	v_pk_mul_f32 v[4:5], v[202:203], v[4:5] op_sel_hi:[0,1]
	v_cvt_pk_f16_f32 v2, v2, v3
	v_cvt_pk_f16_f32 v3, v4, v5
	v_pk_add_f32 v[4:5], v[78:79], v[10:11]
	v_pk_add_f32 v[6:7], v[80:81], v[12:13]
	v_pk_mul_f32 v[4:5], v[202:203], v[4:5] op_sel_hi:[0,1]
	v_pk_mul_f32 v[6:7], v[202:203], v[6:7] op_sel_hi:[0,1]
	v_pk_add_f32 v[44:45], v[68:69], v[64:65]
	v_cvt_pk_f16_f32 v4, v4, v5
	v_cvt_pk_f16_f32 v5, v6, v7
	s_waitcnt vmcnt(0)
	v_pk_add_f32 v[6:7], v[34:35], v[30:31]
	v_pk_add_f32 v[8:9], v[36:37], v[32:33]
	v_pk_mul_f32 v[42:43], v[202:203], v[42:43] op_sel_hi:[0,1]
	v_pk_mul_f32 v[44:45], v[202:203], v[44:45] op_sel_hi:[0,1]
	v_pk_mul_f32 v[6:7], v[202:203], v[6:7] op_sel_hi:[0,1]
	v_pk_mul_f32 v[8:9], v[202:203], v[8:9] op_sel_hi:[0,1]
	v_cvt_pk_f16_f32 v42, v42, v43
	v_cvt_pk_f16_f32 v43, v44, v45
	v_cvt_pk_f16_f32 v6, v6, v7
	v_cvt_pk_f16_f32 v7, v8, v9
	ds_write2_b64 v155, v[38:39], v[42:43] offset0:20 offset1:22
	v_pk_add_f32 v[38:39], v[66:67], v[46:47]
	v_pk_add_f32 v[42:43], v[68:69], v[48:49]
	ds_write2_b64 v155, v[2:3], v[6:7] offset0:28 offset1:30
	v_pk_add_f32 v[2:3], v[34:35], v[14:15]
	v_pk_add_f32 v[6:7], v[36:37], v[16:17]
	v_pk_mul_f32 v[38:39], v[202:203], v[38:39] op_sel_hi:[0,1]
	v_pk_mul_f32 v[42:43], v[202:203], v[42:43] op_sel_hi:[0,1]
	v_pk_mul_f32 v[2:3], v[202:203], v[2:3] op_sel_hi:[0,1]
	v_pk_mul_f32 v[6:7], v[202:203], v[6:7] op_sel_hi:[0,1]
	v_cvt_pk_f16_f32 v38, v38, v39
	v_cvt_pk_f16_f32 v39, v42, v43
	v_cvt_pk_f16_f32 v2, v2, v3
	v_cvt_pk_f16_f32 v3, v6, v7
	ds_write2_b64 v176, v[40:41], v[38:39] offset0:84 offset1:86
	ds_write2_b64 v176, v[4:5], v[2:3] offset0:92 offset1:94
	s_and_saveexec_b64 s[4:5], s[6:7]
	v_lshl_add_u32 v2, v0, 2, 0
	v_add_u32_e32 v2, 0x20800, v2
	v_mov_b32_e32 v3, 0
	ds_write_b32 v2, v3
	s_or_b64 exec, exec, s[4:5]
	s_waitcnt lgkmcnt(0)
	s_barrier
	s_mov_b64 s[4:5], -1
	s_and_b64 vcc, exec, s[22:23]
	s_cbranch_vccnz .LBB1_7
	s_andn2_b64 vcc, exec, s[4:5]
	s_cbranch_vccz .LBB1_14

.LBB1_7:
	s_and_b64 s[4:5], s[20:21], exec
	s_cselect_b32 s4, s13, s15
	s_cselect_b32 s5, s12, s14
	s_lshr_b32 s6, s3, 11
	s_lshl_b32 s2, s2, 14
	s_and_b32 s2, s2, 0x3c000
	s_lshl_b32 s3, s6, 21
	s_or_b32 s2, s3, s2
	s_add_u32 s7, s5, s2
	s_mov_b32 s3, 0
	s_addc_u32 s8, s4, 0
	s_lshl_b32 s12, s29, 1
	s_lshr_b32 s9, s30, 8
	s_andn2_b64 vcc, exec, s[18:19]
	s_mov_b64 s[4:5], -1
	s_cbranch_vccnz .LBB1_9
	v_and_b32_e32 v20, 15, v0
	s_lshl_b32 s13, s9, 6
	v_or_b32_e32 v2, s13, v20
	s_movk_i32 s15, 0x410
	s_and_b32 s14, s12, 6
	v_mul_lo_u32 v2, v2, s15
	v_add_u32_e32 v34, 0, v2
	s_lshl_b32 s18, s14, 7
	v_and_b32_e32 v22, 48, v0
	s_lshl_b32 s2, s14, 5
	v_add3_u32 v8, v34, s18, v22
	s_add_i32 s2, s2, s9
	ds_read_b128 v[2:5], v8
	s_lshl_b64 s[4:5], s[2:3], 13
	s_add_u32 s4, s7, s4
	s_addc_u32 s5, s8, s5
	v_lshlrev_b32_e32 v24, 6, v20
	v_mov_b32_e32 v25, 0
	v_lshl_add_u64 v[6:7], s[4:5], 0, v[24:25]
	v_mov_b32_e32 v23, v25
	v_lshl_add_u64 v[10:11], v[6:7], 0, v[22:23]
	s_waitcnt lgkmcnt(0)
	global_store_dwordx4 v[10:11], v[2:5], off sc1
	v_or_b32_e32 v10, 16, v20
	ds_read_b128 v[6:9], v8 offset:64
	v_or_b32_e32 v2, s13, v10
	v_mul_lo_u32 v2, v2, s15
	v_add_u32_e32 v35, 0, v2
	v_add3_u32 v12, v35, s18, v22
	ds_read_b128 v[2:5], v12
	v_lshlrev_b32_e32 v26, 6, v10
	v_mov_b32_e32 v27, v25
	v_lshl_add_u64 v[10:11], s[4:5], 0, v[26:27]
	v_lshl_add_u64 v[14:15], v[10:11], 0, v[22:23]
	s_waitcnt lgkmcnt(0)
	global_store_dwordx4 v[14:15], v[2:5], off sc1
	v_or_b32_e32 v14, 32, v20
	ds_read_b128 v[10:13], v12 offset:64
	v_or_b32_e32 v2, s13, v14
	v_mul_lo_u32 v2, v2, s15
	v_add_u32_e32 v36, 0, v2
	v_add3_u32 v16, v36, s18, v22
	ds_read_b128 v[2:5], v16
	v_lshlrev_b32_e32 v28, 6, v14
	v_mov_b32_e32 v29, v25
	v_lshl_add_u64 v[14:15], s[4:5], 0, v[28:29]
	v_lshl_add_u64 v[18:19], v[14:15], 0, v[22:23]
	s_waitcnt lgkmcnt(0)
	global_store_dwordx4 v[18:19], v[2:5], off sc1
	v_or_b32_e32 v18, 48, v20
	ds_read_b128 v[14:17], v16 offset:64
	v_or_b32_e32 v2, s13, v18
	v_mul_lo_u32 v2, v2, s15
	v_add_u32_e32 v37, 0, v2
	v_add3_u32 v20, v37, s18, v22
	ds_read_b128 v[2:5], v20
	v_lshlrev_b32_e32 v30, 6, v18
	v_mov_b32_e32 v31, v25
	v_lshl_add_u64 v[18:19], s[4:5], 0, v[30:31]
	s_add_u32 s4, s4, 0x1000
	v_lshl_add_u64 v[32:33], v[18:19], 0, v[22:23]
	s_addc_u32 s5, s5, 0
	s_waitcnt lgkmcnt(0)
	global_store_dwordx4 v[32:33], v[2:5], off sc1
	ds_read_b128 v[18:21], v20 offset:64
	s_or_b32 s2, s14, 1
	v_lshl_add_u64 v[2:3], s[4:5], 0, v[24:25]
	v_lshl_add_u64 v[2:3], v[2:3], 0, v[22:23]
	global_store_dwordx4 v[2:3], v[6:9], off sc1
	v_lshl_add_u64 v[2:3], s[4:5], 0, v[26:27]
	v_lshl_add_u64 v[2:3], v[2:3], 0, v[22:23]
	global_store_dwordx4 v[2:3], v[10:13], off sc1
	v_lshl_add_u64 v[2:3], s[4:5], 0, v[28:29]
	v_lshl_add_u64 v[2:3], v[2:3], 0, v[22:23]
	global_store_dwordx4 v[2:3], v[14:17], off sc1
	v_lshl_add_u64 v[2:3], s[4:5], 0, v[30:31]
	s_lshl_b32 s4, s2, 7
	s_lshl_b32 s2, s2, 5
	s_add_i32 s2, s2, s9
	v_lshl_add_u64 v[2:3], v[2:3], 0, v[22:23]
	v_add3_u32 v10, v34, s4, v22
	s_lshl_b64 s[2:3], s[2:3], 13
	s_waitcnt lgkmcnt(0)
	global_store_dwordx4 v[2:3], v[18:21], off sc1
	ds_read_b128 v[2:5], v10
	s_add_u32 s2, s7, s2
	s_addc_u32 s3, s8, s3
	v_lshl_add_u64 v[6:7], s[2:3], 0, v[24:25]
	v_add3_u32 v16, v35, s4, v22
	v_lshl_add_u64 v[14:15], v[6:7], 0, v[22:23]
	ds_read_b128 v[6:9], v16
	ds_read_b128 v[10:13], v10 offset:64
	s_waitcnt lgkmcnt(2)
	global_store_dwordx4 v[14:15], v[2:5], off sc1
	v_add3_u32 v18, v36, s4, v22
	v_add3_u32 v34, v37, s4, v22
	v_lshl_add_u64 v[2:3], s[2:3], 0, v[26:27]
	v_lshl_add_u64 v[14:15], v[2:3], 0, v[22:23]
	ds_read_b128 v[2:5], v16 offset:64
	s_waitcnt lgkmcnt(2)
	global_store_dwordx4 v[14:15], v[6:9], off sc1
	ds_read_b128 v[6:9], v18
	v_lshl_add_u64 v[14:15], s[2:3], 0, v[28:29]
	v_lshl_add_u64 v[32:33], v[14:15], 0, v[22:23]
	ds_read_b128 v[14:17], v34
	ds_read_b128 v[18:21], v18 offset:64
	s_mov_b64 s[4:5], 0
	s_waitcnt lgkmcnt(2)
	global_store_dwordx4 v[32:33], v[6:9], off sc1
	s_nop 1
	v_lshl_add_u64 v[6:7], s[2:3], 0, v[30:31]
	s_add_u32 s2, s2, 0x1000
	v_lshl_add_u64 v[32:33], v[6:7], 0, v[22:23]
	s_addc_u32 s3, s3, 0
	s_waitcnt lgkmcnt(1)
	global_store_dwordx4 v[32:33], v[14:17], off sc1
	ds_read_b128 v[6:9], v34 offset:64
	s_nop 0
	v_lshl_add_u64 v[14:15], s[2:3], 0, v[24:25]
	v_lshl_add_u64 v[14:15], v[14:15], 0, v[22:23]
	global_store_dwordx4 v[14:15], v[10:13], off sc1
	s_nop 1
	v_lshl_add_u64 v[10:11], s[2:3], 0, v[26:27]
	v_lshl_add_u64 v[10:11], v[10:11], 0, v[22:23]
	global_store_dwordx4 v[10:11], v[2:5], off sc1
	s_nop 1
	v_lshl_add_u64 v[2:3], s[2:3], 0, v[28:29]
	v_lshl_add_u64 v[2:3], v[2:3], 0, v[22:23]
	s_waitcnt lgkmcnt(1)
	global_store_dwordx4 v[2:3], v[18:21], off sc1
	v_lshl_add_u64 v[2:3], s[2:3], 0, v[30:31]
	v_lshl_add_u64 v[2:3], v[2:3], 0, v[22:23]
	s_waitcnt lgkmcnt(0)
	global_store_dwordx4 v[2:3], v[6:9], off sc1
.LBB1_9:
	s_andn2_b64 vcc, exec, s[4:5]
	s_cbranch_vccnz .LBB1_13
	v_lshl_or_b32 v2, s9, 6, v1
	s_movk_i32 s13, 0x410
	v_mul_lo_u32 v2, v2, s13
	v_add_u32_e32 v22, 0, v2
	s_and_b32 s12, s12, 6
	v_lshl_add_u32 v23, s12, 7, v22
	s_lshl_b32 s2, s12, 5
	ds_read_b128 v[2:5], v23
	ds_read_b128 v[6:9], v23 offset:16
	ds_read_b128 v[10:13], v23 offset:32
	ds_read_b128 v[14:17], v23 offset:48
	s_mov_b32 s3, 0
	s_add_i32 s2, s2, s9
	s_lshl_b64 s[4:5], s[2:3], 13
	s_add_u32 s4, s7, s4
	s_addc_u32 s5, s8, s5
	v_lshlrev_b32_e32 v18, 4, v1
	s_waitcnt lgkmcnt(3)
	global_store_dwordx4 v18, v[2:5], s[4:5] sc1
	s_waitcnt lgkmcnt(2)
	global_store_dwordx4 v18, v[6:9], s[4:5] offset:1024 sc1
	s_waitcnt lgkmcnt(1)
	global_store_dwordx4 v18, v[10:13], s[4:5] offset:2048 sc1
	s_waitcnt lgkmcnt(0)
	global_store_dwordx4 v18, v[14:17], s[4:5] offset:3072 sc1
	ds_read_b128 v[2:5], v23 offset:64
	ds_read_b128 v[6:9], v23 offset:80
	ds_read_b128 v[10:13], v23 offset:96
	ds_read_b128 v[14:17], v23 offset:112
	v_mov_b32_e32 v19, 0
	v_lshl_add_u64 v[20:21], s[4:5], 0, v[18:19]
	s_movk_i32 s4, 0x1000
	v_add_co_u32_e32 v20, vcc, s4, v20
	s_or_b32 s2, s12, 1
	s_nop 0
	v_addc_co_u32_e32 v21, vcc, 0, v21, vcc
	s_waitcnt lgkmcnt(3)
	global_store_dwordx4 v[20:21], v[2:5], off sc1
	s_waitcnt lgkmcnt(2)
	global_store_dwordx4 v[20:21], v[6:9], off offset:1024 sc1
	s_waitcnt lgkmcnt(1)
	global_store_dwordx4 v[20:21], v[10:13], off offset:2048 sc1
	s_waitcnt lgkmcnt(0)
	global_store_dwordx4 v[20:21], v[14:17], off offset:3072 sc1
	v_lshl_add_u32 v22, s2, 7, v22
	s_lshl_b32 s2, s2, 5
	ds_read_b128 v[2:5], v22
	ds_read_b128 v[6:9], v22 offset:16
	ds_read_b128 v[10:13], v22 offset:32
	ds_read_b128 v[14:17], v22 offset:48
	s_add_i32 s2, s2, s9
	s_lshl_b64 s[2:3], s[2:3], 13
	s_add_u32 s2, s7, s2
	s_addc_u32 s3, s8, s3
	s_waitcnt lgkmcnt(3)
	global_store_dwordx4 v18, v[2:5], s[2:3] sc1
	s_waitcnt lgkmcnt(2)
	global_store_dwordx4 v18, v[6:9], s[2:3] offset:1024 sc1
	s_waitcnt lgkmcnt(1)
	global_store_dwordx4 v18, v[10:13], s[2:3] offset:2048 sc1
	s_waitcnt lgkmcnt(0)
	global_store_dwordx4 v18, v[14:17], s[2:3] offset:3072 sc1
	ds_read_b128 v[2:5], v22 offset:64
	ds_read_b128 v[6:9], v22 offset:80
	ds_read_b128 v[10:13], v22 offset:96
	ds_read_b128 v[14:17], v22 offset:112
	v_lshl_add_u64 v[20:21], s[2:3], 0, v[18:19]
	v_add_co_u32_e32 v18, vcc, s4, v20
	s_nop 1
	v_addc_co_u32_e32 v19, vcc, 0, v21, vcc
	s_waitcnt lgkmcnt(3)
	global_store_dwordx4 v[18:19], v[2:5], off sc1
	s_waitcnt lgkmcnt(2)
	global_store_dwordx4 v[18:19], v[6:9], off offset:1024 sc1
	s_waitcnt lgkmcnt(1)
	global_store_dwordx4 v[18:19], v[10:13], off offset:2048 sc1
	s_waitcnt lgkmcnt(0)
	global_store_dwordx4 v[18:19], v[14:17], off offset:3072 sc1
	v_and_b32_e32 v2, 7, v0
	v_lshl_add_u32 v18, v2, 7, 0
	v_lshl_add_u32 v6, v2, 2, 0
	v_lshrrev_b32_e32 v2, 3, v0
	v_mad_u32_u24 v19, v2, s13, v18
	ds_read_b128 v[2:5], v19
	v_add_u32_e32 v20, 0x20800, v6
	ds_read_b128 v[6:9], v19 offset:16
	ds_read_b128 v[10:13], v19 offset:32
	ds_read_b128 v[14:17], v19 offset:48
	s_waitcnt lgkmcnt(3)
	v_fma_mix_f32 v21, v2, v2, 0 op_sel_hi:[1,1,0]
	s_nop 0
	v_fma_mix_f32 v2, v2, v2, v21 op_sel:[1,1,0] op_sel_hi:[1,1,0]
	s_nop 0
	v_fma_mix_f32 v2, v3, v3, v2 op_sel_hi:[1,1,0]
	s_nop 0
	v_fma_mix_f32 v2, v3, v3, v2 op_sel:[1,1,0] op_sel_hi:[1,1,0]
	s_nop 0
	v_fma_mix_f32 v2, v4, v4, v2 op_sel_hi:[1,1,0]
	s_nop 0
	v_fma_mix_f32 v2, v4, v4, v2 op_sel:[1,1,0] op_sel_hi:[1,1,0]
	s_nop 0
	v_fma_mix_f32 v2, v5, v5, v2 op_sel_hi:[1,1,0]
	s_nop 0
	v_fma_mix_f32 v2, v5, v5, v2 op_sel:[1,1,0] op_sel_hi:[1,1,0]
	s_waitcnt lgkmcnt(2)
	v_fma_mix_f32 v2, v6, v6, v2 op_sel_hi:[1,1,0]
	s_nop 0
	v_fma_mix_f32 v2, v6, v6, v2 op_sel:[1,1,0] op_sel_hi:[1,1,0]
	s_nop 0
	v_fma_mix_f32 v2, v7, v7, v2 op_sel_hi:[1,1,0]
	s_nop 0
	v_fma_mix_f32 v2, v7, v7, v2 op_sel:[1,1,0] op_sel_hi:[1,1,0]
	s_nop 0
	v_fma_mix_f32 v2, v8, v8, v2 op_sel_hi:[1,1,0]
	s_nop 0
	v_fma_mix_f32 v2, v8, v8, v2 op_sel:[1,1,0] op_sel_hi:[1,1,0]
	s_nop 0
	v_fma_mix_f32 v2, v9, v9, v2 op_sel_hi:[1,1,0]
	s_nop 0
	v_fma_mix_f32 v2, v9, v9, v2 op_sel:[1,1,0] op_sel_hi:[1,1,0]
	s_waitcnt lgkmcnt(1)
	v_fma_mix_f32 v2, v10, v10, v2 op_sel_hi:[1,1,0]
	s_nop 0
	v_fma_mix_f32 v2, v10, v10, v2 op_sel:[1,1,0] op_sel_hi:[1,1,0]
	s_nop 0
	v_fma_mix_f32 v2, v11, v11, v2 op_sel_hi:[1,1,0]
	s_nop 0
	v_fma_mix_f32 v2, v11, v11, v2 op_sel:[1,1,0] op_sel_hi:[1,1,0]
	s_nop 0
	v_fma_mix_f32 v2, v12, v12, v2 op_sel_hi:[1,1,0]
	s_nop 0
	v_fma_mix_f32 v2, v12, v12, v2 op_sel:[1,1,0] op_sel_hi:[1,1,0]
	s_nop 0
	v_fma_mix_f32 v2, v13, v13, v2 op_sel_hi:[1,1,0]
	s_nop 0
	v_fma_mix_f32 v2, v13, v13, v2 op_sel:[1,1,0] op_sel_hi:[1,1,0]
	s_waitcnt lgkmcnt(0)
	v_fma_mix_f32 v2, v14, v14, v2 op_sel_hi:[1,1,0]
	s_nop 0
	v_fma_mix_f32 v2, v14, v14, v2 op_sel:[1,1,0] op_sel_hi:[1,1,0]
	s_nop 0
	v_fma_mix_f32 v2, v15, v15, v2 op_sel_hi:[1,1,0]
	s_nop 0
	v_fma_mix_f32 v2, v15, v15, v2 op_sel:[1,1,0] op_sel_hi:[1,1,0]
	s_nop 0
	v_fma_mix_f32 v6, v16, v16, v2 op_sel_hi:[1,1,0]
	ds_read_b128 v[2:5], v19 offset:64
	v_fma_mix_f32 v6, v16, v16, v6 op_sel:[1,1,0] op_sel_hi:[1,1,0]
	s_nop 0
	v_fma_mix_f32 v6, v17, v17, v6 op_sel_hi:[1,1,0]
	s_nop 0
	v_fma_mix_f32 v10, v17, v17, v6 op_sel:[1,1,0] op_sel_hi:[1,1,0]
	ds_read_b128 v[6:9], v19 offset:80
	s_waitcnt lgkmcnt(1)
	v_fma_mix_f32 v10, v2, v2, v10 op_sel_hi:[1,1,0]
	s_nop 0
	v_fma_mix_f32 v2, v2, v2, v10 op_sel:[1,1,0] op_sel_hi:[1,1,0]
	s_nop 0
	v_fma_mix_f32 v2, v3, v3, v2 op_sel_hi:[1,1,0]
	s_nop 0
	v_fma_mix_f32 v2, v3, v3, v2 op_sel:[1,1,0] op_sel_hi:[1,1,0]
	s_nop 0
	v_fma_mix_f32 v2, v4, v4, v2 op_sel_hi:[1,1,0]
	s_nop 0
	v_fma_mix_f32 v2, v4, v4, v2 op_sel:[1,1,0] op_sel_hi:[1,1,0]
	s_nop 0
	v_fma_mix_f32 v2, v5, v5, v2 op_sel_hi:[1,1,0]
	s_nop 0
	v_fma_mix_f32 v2, v5, v5, v2 op_sel:[1,1,0] op_sel_hi:[1,1,0]
	s_waitcnt lgkmcnt(0)
	v_fma_mix_f32 v2, v6, v6, v2 op_sel_hi:[1,1,0]
	s_nop 0
	v_fma_mix_f32 v2, v6, v6, v2 op_sel:[1,1,0] op_sel_hi:[1,1,0]
	s_nop 0
	v_fma_mix_f32 v2, v7, v7, v2 op_sel_hi:[1,1,0]
	s_nop 0
	v_fma_mix_f32 v2, v7, v7, v2 op_sel:[1,1,0] op_sel_hi:[1,1,0]
	s_nop 0
	v_fma_mix_f32 v6, v8, v8, v2 op_sel_hi:[1,1,0]
	ds_read_b128 v[2:5], v19 offset:96
	v_fma_mix_f32 v6, v8, v8, v6 op_sel:[1,1,0] op_sel_hi:[1,1,0]
	s_nop 0
	v_fma_mix_f32 v6, v9, v9, v6 op_sel_hi:[1,1,0]
	s_nop 0
	v_fma_mix_f32 v10, v9, v9, v6 op_sel:[1,1,0] op_sel_hi:[1,1,0]
	ds_read_b128 v[6:9], v19 offset:112
	s_waitcnt lgkmcnt(1)
	v_fma_mix_f32 v10, v2, v2, v10 op_sel_hi:[1,1,0]
	s_nop 0
	v_fma_mix_f32 v2, v2, v2, v10 op_sel:[1,1,0] op_sel_hi:[1,1,0]
	s_nop 0
	v_fma_mix_f32 v2, v3, v3, v2 op_sel_hi:[1,1,0]
	s_nop 0
	v_fma_mix_f32 v2, v3, v3, v2 op_sel:[1,1,0] op_sel_hi:[1,1,0]
	s_nop 0
	v_fma_mix_f32 v2, v4, v4, v2 op_sel_hi:[1,1,0]
	s_nop 0
	v_fma_mix_f32 v2, v4, v4, v2 op_sel:[1,1,0] op_sel_hi:[1,1,0]
	s_nop 0
	v_fma_mix_f32 v2, v5, v5, v2 op_sel_hi:[1,1,0]
	s_nop 0
	v_fma_mix_f32 v2, v5, v5, v2 op_sel:[1,1,0] op_sel_hi:[1,1,0]
	s_waitcnt lgkmcnt(0)
	v_fma_mix_f32 v2, v6, v6, v2 op_sel_hi:[1,1,0]
	s_nop 0
	v_fma_mix_f32 v2, v6, v6, v2 op_sel:[1,1,0] op_sel_hi:[1,1,0]
	s_nop 0
	v_fma_mix_f32 v2, v7, v7, v2 op_sel_hi:[1,1,0]
	s_nop 0
	v_fma_mix_f32 v2, v7, v7, v2 op_sel:[1,1,0] op_sel_hi:[1,1,0]
	s_nop 0
	v_fma_mix_f32 v2, v8, v8, v2 op_sel_hi:[1,1,0]
	s_nop 0
	v_fma_mix_f32 v2, v8, v8, v2 op_sel:[1,1,0] op_sel_hi:[1,1,0]
	s_nop 0
	v_fma_mix_f32 v2, v9, v9, v2 op_sel_hi:[1,1,0]
	s_nop 0
	v_fma_mix_f32 v2, v9, v9, v2 op_sel:[1,1,0] op_sel_hi:[1,1,0]
	ds_max_u32 v20, v2
	v_or_b32_e32 v2, 0x200, v0
	v_lshrrev_b32_e32 v2, 3, v2
	v_mad_u32_u24 v18, v2, s13, v18
	ds_read_b128 v[2:5], v18
	ds_read_b128 v[6:9], v18 offset:16
	ds_read_b128 v[10:13], v18 offset:32
	ds_read_b128 v[14:17], v18 offset:48
	s_waitcnt lgkmcnt(3)
	v_fma_mix_f32 v19, v2, v2, 0 op_sel_hi:[1,1,0]
	s_nop 0
	v_fma_mix_f32 v2, v2, v2, v19 op_sel:[1,1,0] op_sel_hi:[1,1,0]
	s_nop 0
	v_fma_mix_f32 v2, v3, v3, v2 op_sel_hi:[1,1,0]
	s_nop 0
	v_fma_mix_f32 v2, v3, v3, v2 op_sel:[1,1,0] op_sel_hi:[1,1,0]
	s_nop 0
	v_fma_mix_f32 v2, v4, v4, v2 op_sel_hi:[1,1,0]
	s_nop 0
	v_fma_mix_f32 v2, v4, v4, v2 op_sel:[1,1,0] op_sel_hi:[1,1,0]
	s_nop 0
	v_fma_mix_f32 v2, v5, v5, v2 op_sel_hi:[1,1,0]
	s_nop 0
	v_fma_mix_f32 v2, v5, v5, v2 op_sel:[1,1,0] op_sel_hi:[1,1,0]
	s_waitcnt lgkmcnt(2)
	v_fma_mix_f32 v2, v6, v6, v2 op_sel_hi:[1,1,0]
	s_nop 0
	v_fma_mix_f32 v2, v6, v6, v2 op_sel:[1,1,0] op_sel_hi:[1,1,0]
	s_nop 0
	v_fma_mix_f32 v2, v7, v7, v2 op_sel_hi:[1,1,0]
	s_nop 0
	v_fma_mix_f32 v2, v7, v7, v2 op_sel:[1,1,0] op_sel_hi:[1,1,0]
	s_nop 0
	v_fma_mix_f32 v2, v8, v8, v2 op_sel_hi:[1,1,0]
	s_nop 0
	v_fma_mix_f32 v2, v8, v8, v2 op_sel:[1,1,0] op_sel_hi:[1,1,0]
	s_nop 0
	v_fma_mix_f32 v2, v9, v9, v2 op_sel_hi:[1,1,0]
	s_nop 0
	v_fma_mix_f32 v2, v9, v9, v2 op_sel:[1,1,0] op_sel_hi:[1,1,0]
	s_waitcnt lgkmcnt(1)
	v_fma_mix_f32 v2, v10, v10, v2 op_sel_hi:[1,1,0]
	s_nop 0
	v_fma_mix_f32 v2, v10, v10, v2 op_sel:[1,1,0] op_sel_hi:[1,1,0]
	s_nop 0
	v_fma_mix_f32 v2, v11, v11, v2 op_sel_hi:[1,1,0]
	s_nop 0
	v_fma_mix_f32 v2, v11, v11, v2 op_sel:[1,1,0] op_sel_hi:[1,1,0]
	s_nop 0
	v_fma_mix_f32 v2, v12, v12, v2 op_sel_hi:[1,1,0]
	s_nop 0
	v_fma_mix_f32 v2, v12, v12, v2 op_sel:[1,1,0] op_sel_hi:[1,1,0]
	s_nop 0
	v_fma_mix_f32 v2, v13, v13, v2 op_sel_hi:[1,1,0]
	s_nop 0
	v_fma_mix_f32 v2, v13, v13, v2 op_sel:[1,1,0] op_sel_hi:[1,1,0]
	s_waitcnt lgkmcnt(0)
	v_fma_mix_f32 v2, v14, v14, v2 op_sel_hi:[1,1,0]
	s_nop 0
	v_fma_mix_f32 v2, v14, v14, v2 op_sel:[1,1,0] op_sel_hi:[1,1,0]
	s_nop 0
	v_fma_mix_f32 v2, v15, v15, v2 op_sel_hi:[1,1,0]
	s_nop 0
	v_fma_mix_f32 v2, v15, v15, v2 op_sel:[1,1,0] op_sel_hi:[1,1,0]
	s_nop 0
	v_fma_mix_f32 v6, v16, v16, v2 op_sel_hi:[1,1,0]
	ds_read_b128 v[2:5], v18 offset:64
	v_fma_mix_f32 v6, v16, v16, v6 op_sel:[1,1,0] op_sel_hi:[1,1,0]
	s_nop 0
	v_fma_mix_f32 v6, v17, v17, v6 op_sel_hi:[1,1,0]
	s_nop 0
	v_fma_mix_f32 v10, v17, v17, v6 op_sel:[1,1,0] op_sel_hi:[1,1,0]
	ds_read_b128 v[6:9], v18 offset:80
	s_waitcnt lgkmcnt(1)
	v_fma_mix_f32 v10, v2, v2, v10 op_sel_hi:[1,1,0]
	s_nop 0
	v_fma_mix_f32 v2, v2, v2, v10 op_sel:[1,1,0] op_sel_hi:[1,1,0]
	s_nop 0
	v_fma_mix_f32 v2, v3, v3, v2 op_sel_hi:[1,1,0]
	s_nop 0
	v_fma_mix_f32 v2, v3, v3, v2 op_sel:[1,1,0] op_sel_hi:[1,1,0]
	s_nop 0
	v_fma_mix_f32 v2, v4, v4, v2 op_sel_hi:[1,1,0]
	s_nop 0
	v_fma_mix_f32 v2, v4, v4, v2 op_sel:[1,1,0] op_sel_hi:[1,1,0]
	s_nop 0
	v_fma_mix_f32 v2, v5, v5, v2 op_sel_hi:[1,1,0]
	s_nop 0
	v_fma_mix_f32 v2, v5, v5, v2 op_sel:[1,1,0] op_sel_hi:[1,1,0]
	s_waitcnt lgkmcnt(0)
	v_fma_mix_f32 v2, v6, v6, v2 op_sel_hi:[1,1,0]
	s_nop 0
	v_fma_mix_f32 v2, v6, v6, v2 op_sel:[1,1,0] op_sel_hi:[1,1,0]
	s_nop 0
	v_fma_mix_f32 v2, v7, v7, v2 op_sel_hi:[1,1,0]
	s_nop 0
	v_fma_mix_f32 v2, v7, v7, v2 op_sel:[1,1,0] op_sel_hi:[1,1,0]
	s_nop 0
	v_fma_mix_f32 v6, v8, v8, v2 op_sel_hi:[1,1,0]
	ds_read_b128 v[2:5], v18 offset:96
	v_fma_mix_f32 v6, v8, v8, v6 op_sel:[1,1,0] op_sel_hi:[1,1,0]
	s_nop 0
	v_fma_mix_f32 v6, v9, v9, v6 op_sel_hi:[1,1,0]
	s_nop 0
	v_fma_mix_f32 v10, v9, v9, v6 op_sel:[1,1,0] op_sel_hi:[1,1,0]
	ds_read_b128 v[6:9], v18 offset:112
	s_waitcnt lgkmcnt(1)
	v_fma_mix_f32 v10, v2, v2, v10 op_sel_hi:[1,1,0]
	s_nop 0
	v_fma_mix_f32 v2, v2, v2, v10 op_sel:[1,1,0] op_sel_hi:[1,1,0]
	s_nop 0
	v_fma_mix_f32 v2, v3, v3, v2 op_sel_hi:[1,1,0]
	s_nop 0
	v_fma_mix_f32 v2, v3, v3, v2 op_sel:[1,1,0] op_sel_hi:[1,1,0]
	s_nop 0
	v_fma_mix_f32 v2, v4, v4, v2 op_sel_hi:[1,1,0]
	s_nop 0
	v_fma_mix_f32 v2, v4, v4, v2 op_sel:[1,1,0] op_sel_hi:[1,1,0]
	s_nop 0
	v_fma_mix_f32 v2, v5, v5, v2 op_sel_hi:[1,1,0]
	s_nop 0
	v_fma_mix_f32 v2, v5, v5, v2 op_sel:[1,1,0] op_sel_hi:[1,1,0]
	s_waitcnt lgkmcnt(0)
	v_fma_mix_f32 v2, v6, v6, v2 op_sel_hi:[1,1,0]
	s_nop 0
	v_fma_mix_f32 v2, v6, v6, v2 op_sel:[1,1,0] op_sel_hi:[1,1,0]
	s_nop 0
	v_fma_mix_f32 v2, v7, v7, v2 op_sel_hi:[1,1,0]
	s_nop 0
	v_fma_mix_f32 v2, v7, v7, v2 op_sel:[1,1,0] op_sel_hi:[1,1,0]
	s_nop 0
	v_fma_mix_f32 v2, v8, v8, v2 op_sel_hi:[1,1,0]
	s_nop 0
	v_fma_mix_f32 v2, v8, v8, v2 op_sel:[1,1,0] op_sel_hi:[1,1,0]
	s_nop 0
	v_fma_mix_f32 v2, v9, v9, v2 op_sel_hi:[1,1,0]
	s_nop 0
	v_fma_mix_f32 v2, v9, v9, v2 op_sel:[1,1,0] op_sel_hi:[1,1,0]
	ds_max_u32 v20, v2
	s_waitcnt lgkmcnt(0)
	s_barrier
	s_and_saveexec_b64 s[2:3], s[0:1]
	s_cbranch_execz .LBB1_12
	v_lshlrev_b32_e32 v0, 2, v0
	v_add_u32_e32 v2, 0, v0
	v_add_u32_e32 v2, 0x20800, v2
	ds_read_b32 v2, v2
	s_lshl_b32 s0, s6, 5
	s_add_u32 s0, s16, s0
	s_addc_u32 s1, s17, 0
	s_waitcnt lgkmcnt(0)
	global_atomic_umax v0, v2, s[0:1]

.LBB1_14:
	s_lshl_b32 s4, s29, 4
	v_lshlrev_b32_e32 v0, 4, v1
	s_mov_b32 s1, 0
	v_mov_b32_e32 v1, 0
	s_add_i32 s0, s4, s28
	v_lshl_add_u64 v[8:9], s[10:11], 0, v[0:1]
	s_lshl_b64 s[2:3], s[0:1], 10
	v_add_u32_e32 v4, 0, v0
	s_mulk_i32 s29, 0x4100
	v_lshl_add_u64 v[10:11], v[8:9], 0, s[2:3]
	s_or_b32 s2, s4, 1
	v_add_u32_e32 v0, s29, v4
	s_mul_i32 s3, s2, 0x410
	ds_read_b128 v[0:3], v0
	v_add_u32_e32 v12, s3, v4
	ds_read_b128 v[4:7], v12
	s_add_i32 s2, s2, s28
	s_mov_b32 s3, s1
	s_lshl_b64 s[2:3], s[2:3], 10
	s_waitcnt lgkmcnt(1)
	global_store_dwordx4 v[10:11], v[0:3], off sc1
	s_nop 1
	v_lshl_add_u64 v[0:1], v[8:9], 0, s[2:3]
	s_waitcnt lgkmcnt(0)
	global_store_dwordx4 v[0:1], v[4:7], off sc1
	ds_read_b128 v[0:3], v12 offset:1040
	ds_read_b128 v[4:7], v12 offset:2080
	s_add_i32 s2, s0, 2
	s_mov_b32 s3, s1
	s_lshl_b64 s[2:3], s[2:3], 10
	v_lshl_add_u64 v[10:11], v[8:9], 0, s[2:3]
	s_add_i32 s2, s0, 3
	s_mov_b32 s3, s1
	s_lshl_b64 s[2:3], s[2:3], 10
	s_waitcnt lgkmcnt(1)
	global_store_dwordx4 v[10:11], v[0:3], off sc1
	s_nop 1
	v_lshl_add_u64 v[0:1], v[8:9], 0, s[2:3]
	s_waitcnt lgkmcnt(0)
	global_store_dwordx4 v[0:1], v[4:7], off sc1
	ds_read_b128 v[0:3], v12 offset:3120
	ds_read_b128 v[4:7], v12 offset:4160
	s_add_i32 s2, s0, 4
	s_mov_b32 s3, s1
	s_lshl_b64 s[2:3], s[2:3], 10
	v_lshl_add_u64 v[10:11], v[8:9], 0, s[2:3]
	s_add_i32 s2, s0, 5
	s_mov_b32 s3, s1
	s_lshl_b64 s[2:3], s[2:3], 10
	s_waitcnt lgkmcnt(1)
	global_store_dwordx4 v[10:11], v[0:3], off sc1
	s_nop 1
	v_lshl_add_u64 v[0:1], v[8:9], 0, s[2:3]
	s_waitcnt lgkmcnt(0)
	global_store_dwordx4 v[0:1], v[4:7], off sc1
	ds_read_b128 v[0:3], v12 offset:5200
	ds_read_b128 v[4:7], v12 offset:6240
	s_add_i32 s2, s0, 6
	s_mov_b32 s3, s1
	s_lshl_b64 s[2:3], s[2:3], 10
	v_lshl_add_u64 v[10:11], v[8:9], 0, s[2:3]
	s_add_i32 s2, s0, 7
	s_mov_b32 s3, s1
	s_lshl_b64 s[2:3], s[2:3], 10
	s_waitcnt lgkmcnt(1)
	global_store_dwordx4 v[10:11], v[0:3], off sc1
	s_nop 1
	v_lshl_add_u64 v[0:1], v[8:9], 0, s[2:3]
	s_waitcnt lgkmcnt(0)
	global_store_dwordx4 v[0:1], v[4:7], off sc1
	ds_read_b128 v[0:3], v12 offset:7280
	ds_read_b128 v[4:7], v12 offset:8320
	s_add_i32 s2, s0, 8
	s_mov_b32 s3, s1
	s_lshl_b64 s[2:3], s[2:3], 10
	v_lshl_add_u64 v[10:11], v[8:9], 0, s[2:3]
	s_add_i32 s2, s0, 9
	s_mov_b32 s3, s1
	s_lshl_b64 s[2:3], s[2:3], 10
	s_waitcnt lgkmcnt(1)
	global_store_dwordx4 v[10:11], v[0:3], off sc1
	s_nop 1
	v_lshl_add_u64 v[0:1], v[8:9], 0, s[2:3]
	s_waitcnt lgkmcnt(0)
	global_store_dwordx4 v[0:1], v[4:7], off sc1
	ds_read_b128 v[0:3], v12 offset:9360
	ds_read_b128 v[4:7], v12 offset:10400
	s_add_i32 s2, s0, 10
	s_mov_b32 s3, s1
	s_lshl_b64 s[2:3], s[2:3], 10
	v_lshl_add_u64 v[10:11], v[8:9], 0, s[2:3]
	s_add_i32 s2, s0, 11
	s_mov_b32 s3, s1
	s_lshl_b64 s[2:3], s[2:3], 10
	s_waitcnt lgkmcnt(1)
	global_store_dwordx4 v[10:11], v[0:3], off sc1
	s_nop 1
	v_lshl_add_u64 v[0:1], v[8:9], 0, s[2:3]
	s_waitcnt lgkmcnt(0)
	global_store_dwordx4 v[0:1], v[4:7], off sc1
	ds_read_b128 v[0:3], v12 offset:11440
	ds_read_b128 v[4:7], v12 offset:12480
	s_add_i32 s2, s0, 12
	s_mov_b32 s3, s1
	s_lshl_b64 s[2:3], s[2:3], 10
	v_lshl_add_u64 v[10:11], v[8:9], 0, s[2:3]
	s_add_i32 s2, s0, 13
	s_mov_b32 s3, s1
	s_lshl_b64 s[2:3], s[2:3], 10
	s_waitcnt lgkmcnt(1)
	global_store_dwordx4 v[10:11], v[0:3], off sc1
	s_nop 1
	v_lshl_add_u64 v[0:1], v[8:9], 0, s[2:3]
	s_waitcnt lgkmcnt(0)
	global_store_dwordx4 v[0:1], v[4:7], off sc1
	ds_read_b128 v[0:3], v12 offset:13520
	ds_read_b128 v[4:7], v12 offset:14560
	s_add_i32 s2, s0, 14
	s_mov_b32 s3, s1
	s_lshl_b64 s[2:3], s[2:3], 10
	s_add_i32 s0, s0, 15
	v_lshl_add_u64 v[10:11], v[8:9], 0, s[2:3]
	s_lshl_b64 s[0:1], s[0:1], 10
	s_waitcnt lgkmcnt(1)
	global_store_dwordx4 v[10:11], v[0:3], off sc1
	s_nop 1
	v_lshl_add_u64 v[0:1], v[8:9], 0, s[0:1]
	s_waitcnt lgkmcnt(0)
	global_store_dwordx4 v[0:1], v[4:7], off sc1
	s_endpgm

.LBB2_4:
	s_and_b32 s0, s23, 0x3fffffc0
	s_lshl_b32 s0, s0, 2
	s_lshl_b64 s[10:11], s[2:3], 9
	s_add_i32 s23, s0, 0
	s_add_u32 s0, s14, 0x6000
	s_waitcnt vmcnt(0) lgkmcnt(0)
	s_barrier
	s_addc_u32 s1, s15, 0
	s_mov_b32 s2, m0
	s_mov_b32 m0, s24
	s_nop 0
	global_load_lds_dwordx4 v189, s[0:1]
	s_mov_b32 m0, s2
	s_add_u32 s0, s12, 0x2000
	s_addc_u32 s1, s13, 0
	s_cmp_lg_u32 0, -1
	s_cselect_b32 s2, 0, 0
	s_add_i32 s2, s2, s22
	s_add_i32 s2, s2, 0x8000
	s_mov_b32 s4, m0
	s_mov_b32 m0, s2
	s_nop 0
	global_load_lds_dwordx4 v189, s[0:1]
	s_mov_b32 m0, s4
	ds_read_b128 v[172:175], v190 offset:8192
	ds_read_b128 v[168:171], v190 offset:8704
	ds_read_b128 v[164:167], v190 offset:10240
	ds_read_b128 v[160:163], v190 offset:10752
	ds_read_b128 v[156:159], v190 offset:12288
	ds_read_b128 v[152:155], v190 offset:12800
	ds_read_b128 v[148:151], v190 offset:14336
	ds_read_b128 v[144:147], v190 offset:14848
	s_mov_b32 s3, 0
	s_add_i32 s2, s28, s27
	s_lshl_b64 s[4:5], s[2:3], 18
	v_lshlrev_b32_e32 v2, 1, v1
	v_lshlrev_b32_e32 v3, 3, v0
	s_add_u32 s2, s8, s4
	v_and_b32_e32 v2, 32, v2
	v_and_b32_e32 v3, 24, v3
	v_lshlrev_b32_e32 v185, 4, v0
	s_waitcnt vmcnt(2) lgkmcnt(0)
	s_barrier
	s_addc_u32 s4, s9, s5
	v_add3_u32 v2, 0, v2, v3
	v_lshlrev_b32_e32 v3, 8, v18
	v_and_b32_e32 v0, 0xc0, v185
	s_add_u32 s27, s2, 0x2000
	v_mov_b32_e32 v188, 0
	v_lshrrev_b32_e32 v183, 4, v1
	v_add3_u32 v187, v2, v3, v0
	s_mov_b32 s26, -1
	v_cmp_gt_u32_e64 s[0:1], 32, v1
	v_lshl_add_u32 v186, v181, 2, s23
	s_addc_u32 s28, s4, 0
	s_movk_i32 s29, 0x4000
	s_movk_i32 s31, 0x2000
	s_mov_b64 s[8:9], 0
	s_mov_b32 s30, 0x41000000
	v_mov_b32_e32 v0, 0
	v_mov_b32_e32 v1, v188
	v_mov_b32_e32 v2, v188
	v_mov_b32_e32 v3, v188
	v_mov_b32_e32 v4, v188
	v_mov_b32_e32 v5, v188
	v_mov_b32_e32 v6, v188
	v_mov_b32_e32 v7, v188
	v_mov_b32_e32 v8, v188
	v_mov_b32_e32 v9, v188
	v_mov_b32_e32 v10, v188
	v_mov_b32_e32 v11, v188
	v_mov_b32_e32 v12, v188
	v_mov_b32_e32 v13, v188
	v_mov_b32_e32 v14, v188
	v_mov_b32_e32 v15, v188
	v_mov_b32_e32 v16, 0
	v_mov_b32_e32 v17, v188
	v_mov_b32_e32 v18, v188
	v_mov_b32_e32 v19, v188
	v_mov_b32_e32 v20, v188
	v_mov_b32_e32 v21, v188
	v_mov_b32_e32 v22, v188
	v_mov_b32_e32 v23, v188
	v_mov_b32_e32 v24, v188
	v_mov_b32_e32 v25, v188
	v_mov_b32_e32 v26, v188
	v_mov_b32_e32 v27, v188
	v_mov_b32_e32 v28, v188
	v_mov_b32_e32 v29, v188
	v_mov_b32_e32 v30, v188
	v_mov_b32_e32 v31, v188
	s_cmp_ge_u32 s20, 4
	s_cbranch_scc0 .Lattn_prio_done
	s_setprio 1
.Lattn_prio_done:
.LBB2_5:
	s_add_i32 s26, s26, 2
	v_add_u32_e32 v191, s3, v187
	ds_read_b64_tr_b16 v[176:177], v191 offset:24576
	ds_read_b64_tr_b16 v[178:179], v191 offset:25088
	s_waitcnt lgkmcnt(0)
	v_mfma_f32_32x32x16_f16 v[96:111], v[172:175], v[124:127], v[32:47]
	v_exp_f32_e32 v56, v56
	v_exp_f32_e32 v57, v57
	v_cvt_pk_f16_f32 v140, v64, v65
	v_cvt_pk_f16_f32 v141, v66, v67
	ds_read_b64_tr_b16 v[172:173], v191 offset:28672
	ds_read_b64_tr_b16 v[174:175], v191 offset:29184
	v_mfma_f32_32x32x16_f16 v[80:95], v[168:171], v[124:127], v[32:47]
	v_exp_f32_e32 v58, v58
	v_exp_f32_e32 v59, v59
	v_pk_add_f16 v128, v140, v141
	v_cvt_pk_f16_f32 v142, v68, v69
	v_cvt_pk_f16_f32 v143, v70, v71
	ds_read_b64_tr_b16 v[64:65], v191 offset:25600
	ds_read_b64_tr_b16 v[66:67], v191 offset:26112
	v_mfma_f32_32x32x16_f16 v[96:111], v[164:167], v[120:123], v[96:111]
	v_exp_f32_e32 v60, v60
	v_exp_f32_e32 v61, v61
	v_pk_add_f16 v129, v142, v143
	v_cvt_pk_f16_f32 v136, v72, v73
	v_cvt_pk_f16_f32 v137, v74, v75
	ds_read_b64_tr_b16 v[68:69], v191 offset:29696
	ds_read_b64_tr_b16 v[70:71], v191 offset:30208
	v_mfma_f32_32x32x16_f16 v[80:95], v[160:163], v[120:123], v[80:95]
	v_exp_f32_e32 v62, v62
	v_exp_f32_e32 v63, v63
	v_pk_add_f16 v72, v136, v137
	v_pk_add_f16 v128, v128, v129
	v_cvt_pk_f16_f32 v138, v76, v77
	v_cvt_pk_f16_f32 v139, v78, v79
	s_min_u32 s2, s26, 28
	s_lshl_b32 s2, s2, 13
	s_add_u32 s2, s14, s2
	s_addc_u32 s3, s15, 0
	s_add_u32 s2, s2, 0x6000
	s_addc_u32 s3, s3, 0
	s_add_i32 s4, s31, s24
	s_mov_b32 s5, m0
	s_mov_b32 m0, s4
	s_nop 0
	global_load_lds_dwordx4 v189, s[2:3]
	s_mov_b32 m0, s5
	ds_read_b64_tr_b16 v[76:77], v191 offset:26624
	ds_read_b64_tr_b16 v[78:79], v191 offset:27136
	v_mfma_f32_32x32x16_f16 v[96:111], v[156:159], v[116:119], v[96:111]
	v_pk_add_f16 v73, v138, v139
	v_cvt_pk_f16_f32 v132, v48, v49
	v_cvt_pk_f16_f32 v133, v50, v51
	ds_read_b64_tr_b16 v[48:49], v191 offset:30720
	ds_read_b64_tr_b16 v[50:51], v191 offset:31232
	v_mfma_f32_32x32x16_f16 v[80:95], v[152:155], v[116:119], v[80:95]
	v_pk_add_f16 v129, v72, v73
	v_cvt_pk_f16_f32 v134, v52, v53
	v_cvt_pk_f16_f32 v135, v54, v55
	v_pk_add_f16 v156, v132, v133
	s_add_u32 s2, s27, 0x2000
	s_addc_u32 s3, s28, 0
	s_add_i32 s4, s29, s25
	s_mov_b32 s5, m0
	s_mov_b32 m0, s4
	s_nop 0
	global_load_lds_dwordx4 v189, s[2:3]
	s_mov_b32 m0, s5
	ds_read_b64_tr_b16 v[72:73], v191 offset:27648
	ds_read_b64_tr_b16 v[74:75], v191 offset:28160
	v_mfma_f32_32x32x16_f16 v[96:111], v[148:151], v[112:115], v[96:111]
	v_pk_add_f16 v153, v128, v129
	v_cvt_pk_f16_f32 v128, v56, v57
	v_cvt_pk_f16_f32 v129, v58, v59
	v_pk_add_f16 v152, v134, v135
	ds_read_b64_tr_b16 v[52:53], v191 offset:31744
	ds_read_b64_tr_b16 v[54:55], v191 offset:32256
	v_mfma_f32_32x32x16_f16 v[80:95], v[144:147], v[112:115], v[80:95]
	v_pk_add_f16 v56, v128, v129
	v_pk_add_f16 v57, v156, v152
	v_cvt_pk_f16_f32 v130, v60, v61
	v_cvt_pk_f16_f32 v131, v62, v63
	v_cndmask_b32_e64 v58, 0, 1, s[18:19]
	v_cmp_ne_u32_e64 s[2:3], 1, v58
	s_andn2_b64 vcc, exec, s[18:19]
	v_pk_add_f16 v57, v153, v57
	v_pk_add_f16 v58, v130, v131
	s_cbranch_vccnz .LBB2_7
	v_pk_add_f16 v59, v56, v58
	v_max3_f32 v61, v96, v97, v80
	v_max3_f32 v62, v98, v99, v81
	s_mov_b64 s[8:9], 0
	v_pk_add_f16 v59, v57, v59
	s_nop 0
	v_cvt_f32_f16_e32 v60, v59
	v_cvt_f32_f16_sdwa v59, v59 dst_sel:DWORD dst_unused:UNUSED_PAD src0_sel:WORD_1
	v_add_f32_e32 v59, v59, v60
	v_add_f32_e32 v188, v188, v59
	v_max3_f32 v59, v61, v82, v83
	v_max3_f32 v60, v62, v102, v103
	s_nop 0
	v_max3_f32 v59, v59, v100, v101
	v_max3_f32 v60, v60, v86, v87
	s_nop 0
	v_max3_f32 v59, v59, v84, v85
	v_max3_f32 v60, v60, v106, v107
	s_nop 0
	v_max3_f32 v59, v59, v104, v105
	v_max3_f32 v60, v60, v90, v91
	s_nop 0
	v_max3_f32 v59, v59, v88, v89
	v_max3_f32 v60, v60, v110, v111
	s_nop 0
	v_max3_f32 v59, v59, v108, v109
	v_max3_f32 v60, v60, v94, v95
	s_nop 0
	v_max3_f32 v59, v59, v92, v93
	s_nop 0
	v_max_f32 v59, v59, v60
	s_nop 0
	v_mov_b32_e32 v60, v59
	s_nop 1
	v_permlane32_swap_b32_e32 v59, v60
	v_max_f32 v59, v59, v60
	s_nop 0
	v_cmp_lt_f32_e32 vcc, s30, v59
	s_cbranch_vccnz .LBB2_19

.LBB2_31:
	v_exp_f32_e32 v49, v40
	v_add_f32_e32 v40, v80, v81
	v_add_f32_e32 v40, v40, v82
	v_add_f32_e32 v40, v40, v83
	v_add_f32_e32 v40, v40, v84
	v_exp_f32_e32 v62, v41
	v_exp_f32_e32 v63, v42
	v_exp_f32_e32 v64, v43
	v_exp_f32_e32 v65, v44
	v_exp_f32_e32 v66, v45
	v_exp_f32_e32 v67, v46
	v_exp_f32_e32 v68, v47
	v_add_f32_e32 v50, v40, v85
	v_cvt_pk_f16_f32 v40, v80, v81
	v_cvt_pk_f16_f32 v41, v82, v83
	v_cvt_pk_f16_f32 v42, v84, v85
	v_cvt_pk_f16_f32 v43, v86, v87
	ds_read_b64_tr_b16 v[44:45], v187 offset:32768
	ds_read_b64_tr_b16 v[46:47], v187 offset:33280
	v_add_f32_e32 v50, v50, v86
	v_add_f32_e32 v54, v50, v87
	ds_read_b64_tr_b16 v[50:51], v187 offset:33792
	ds_read_b64_tr_b16 v[52:53], v187 offset:34304
	s_waitcnt lgkmcnt(2)
	v_mfma_f32_32x32x16_f16 v[0:15], v[40:43], v[44:47], v[0:15]
	ds_read_b64_tr_b16 v[44:45], v187 offset:36864
	ds_read_b64_tr_b16 v[46:47], v187 offset:37376
	v_add_f32_e32 v54, v54, v88
	v_add_f32_e32 v69, v54, v89
	v_cvt_pk_f16_f32 v54, v88, v89
	v_cvt_pk_f16_f32 v55, v90, v91
	v_cvt_pk_f16_f32 v56, v92, v93
	v_cvt_pk_f16_f32 v57, v94, v95
	s_waitcnt lgkmcnt(0)
	v_mfma_f32_32x32x16_f16 v[16:31], v[40:43], v[44:47], v[16:31]
	v_add_f32_e32 v40, v69, v90
	v_add_f32_e32 v40, v40, v91
	v_add_f32_e32 v40, v40, v92
	v_add_f32_e32 v40, v40, v93
	ds_read_b64_tr_b16 v[58:59], v187 offset:37888
	ds_read_b64_tr_b16 v[60:61], v187 offset:38400
	v_add_f32_e32 v40, v40, v94
	v_add_f32_e32 v40, v40, v95
	v_mfma_f32_32x32x16_f16 v[0:15], v[54:57], v[50:53], v[0:15]
	v_add_f32_e32 v40, v40, v32
	v_add_f32_e32 v50, v40, v33
	v_cvt_pk_f16_f32 v40, v32, v33
	v_cvt_pk_f16_f32 v41, v34, v35
	v_cvt_pk_f16_f32 v42, v36, v37
	v_cvt_pk_f16_f32 v43, v38, v39
	ds_read_b64_tr_b16 v[44:45], v187 offset:34816
	ds_read_b64_tr_b16 v[46:47], v187 offset:35328
	s_waitcnt lgkmcnt(2)
	v_mfma_f32_32x32x16_f16 v[16:31], v[54:57], v[58:61], v[16:31]
	v_add_f32_e32 v32, v50, v34
	v_add_f32_e32 v50, v32, v35
	ds_read_b64_tr_b16 v[32:33], v187 offset:35840
	ds_read_b64_tr_b16 v[34:35], v187 offset:36352
	v_add_f32_e32 v36, v50, v36
	v_add_f32_e32 v36, v36, v37
	v_cvt_pk_f16_f32 v50, v49, v62
	v_cvt_pk_f16_f32 v51, v63, v64
	s_waitcnt lgkmcnt(2)
	v_mfma_f32_32x32x16_f16 v[0:15], v[40:43], v[44:47], v[0:15]
	ds_read_b64_tr_b16 v[44:45], v187 offset:38912
	ds_read_b64_tr_b16 v[46:47], v187 offset:39424
	v_cvt_pk_f16_f32 v52, v65, v66
	v_cvt_pk_f16_f32 v53, v67, v68
	ds_read_b64_tr_b16 v[54:55], v187 offset:39936
	ds_read_b64_tr_b16 v[56:57], v187 offset:40448
	v_add_f32_e32 v36, v36, v38
	v_add_f32_e32 v36, v36, v39
	v_add_f32_e32 v36, v36, v49
	s_waitcnt lgkmcnt(2)
	v_mfma_f32_32x32x16_f16 v[16:31], v[40:43], v[44:47], v[16:31]
	v_add_f32_e32 v36, v36, v62
	v_mfma_f32_32x32x16_f16 v[0:15], v[50:53], v[32:35], v[0:15]
	v_add_f32_e32 v32, v36, v63
	v_add_f32_e32 v32, v32, v64
	v_add_f32_e32 v32, v32, v65
	v_add_f32_e32 v32, v32, v66
	v_add_f32_e32 v32, v32, v67
	v_add_f32_e32 v32, v32, v68
	v_add_f32_e32 v32, v188, v32
	s_waitcnt lgkmcnt(0)
	v_mfma_f32_32x32x16_f16 v[16:31], v[50:53], v[54:57], v[16:31]
	v_mov_b32_e32 v33, v32
	s_nop 1
	v_permlane32_swap_b32_e32 v32, v33
	s_and_saveexec_b64 s[2:3], s[0:1]
	v_add_f32_e32 v32, v32, v33
	ds_write_b32 v186, v32 offset:49280
	s_or_b64 exec, exec, s[2:3]
	s_waitcnt lgkmcnt(0)
	ds_read_b128 v[32:35], v48 offset:49280
	ds_read_b128 v[36:39], v48 offset:49312
	s_lshl_b64 s[0:1], s[10:11], 2
	s_add_u32 s0, s6, s0
	s_addc_u32 s1, s7, s1
	s_waitcnt lgkmcnt(1)
	v_rcp_f32_e32 v40, v32
	v_rcp_f32_e32 v41, v33
	s_lshl_b32 s2, s20, 13
	v_rcp_f32_e32 v42, v34
	v_rcp_f32_e32 v43, v35
	s_waitcnt lgkmcnt(0)
	v_rcp_f32_e32 v44, v36
	ds_read_b128 v[32:35], v48 offset:49344
	v_rcp_f32_e32 v45, v37
	v_rcp_f32_e32 v46, v38
	v_rcp_f32_e32 v47, v39
	ds_read_b128 v[36:39], v48 offset:49376
	s_add_i32 s2, s2, 0
	v_lshlrev_b32_e32 v48, 2, v181
	v_add3_u32 v48, s2, v182, v48
	v_mul_f32_e32 v0, v0, v40
	v_mul_f32_e32 v16, v16, v40
	v_add_u32_e32 v40, 0xc800, v48
	ds_write2_b32 v40, v0, v16 offset1:32
	v_mul_f32_e32 v0, v1, v41
	v_mul_f32_e32 v1, v17, v41
	ds_write2_b32 v40, v0, v1 offset0:64 offset1:96
	v_mul_f32_e32 v0, v2, v42
	v_mul_f32_e32 v1, v18, v42
	ds_write2_b32 v40, v0, v1 offset0:128 offset1:160
	v_mul_f32_e32 v0, v3, v43
	v_mul_f32_e32 v1, v19, v43
	s_waitcnt lgkmcnt(4)
	v_rcp_f32_e32 v32, v32
	ds_write2_b32 v40, v0, v1 offset0:192 offset1:224
	v_mul_f32_e32 v0, v4, v44
	v_mul_f32_e32 v1, v20, v44
	v_add_u32_e32 v2, 0xd000, v48
	v_rcp_f32_e32 v33, v33
	ds_write2_b32 v2, v0, v1 offset1:32
	v_mul_f32_e32 v0, v5, v45
	v_mul_f32_e32 v1, v21, v45
	v_rcp_f32_e32 v34, v34
	ds_write2_b32 v2, v0, v1 offset0:64 offset1:96
	v_mul_f32_e32 v0, v6, v46
	v_mul_f32_e32 v1, v22, v46
	v_rcp_f32_e32 v35, v35
	ds_write2_b32 v2, v0, v1 offset0:128 offset1:160
	v_mul_f32_e32 v0, v7, v47
	v_mul_f32_e32 v1, v23, v47
	s_waitcnt lgkmcnt(7)
	v_rcp_f32_e32 v36, v36
	ds_write2_b32 v2, v0, v1 offset0:192 offset1:224
	v_mul_f32_e32 v0, v8, v32
	v_mul_f32_e32 v1, v24, v32
	v_add_u32_e32 v2, 0xd800, v48
	v_rcp_f32_e32 v37, v37
	ds_write2_b32 v2, v0, v1 offset1:32
	v_mul_f32_e32 v0, v9, v33
	v_mul_f32_e32 v1, v25, v33
	v_rcp_f32_e32 v38, v38
	ds_write2_b32 v2, v0, v1 offset0:64 offset1:96
	v_mul_f32_e32 v0, v10, v34
	v_mul_f32_e32 v1, v26, v34
	v_rcp_f32_e32 v39, v39
	ds_write2_b32 v2, v0, v1 offset0:128 offset1:160
	v_mul_f32_e32 v0, v11, v35
	v_mul_f32_e32 v1, v27, v35
	ds_write2_b32 v2, v0, v1 offset0:192 offset1:224
	v_mul_f32_e32 v0, v12, v36
	v_mul_f32_e32 v1, v28, v36
	v_add_u32_e32 v2, 0xe000, v48
	ds_write2_b32 v2, v0, v1 offset1:32
	v_mul_f32_e32 v0, v13, v37
	v_mul_f32_e32 v1, v29, v37
	ds_write2_b32 v2, v0, v1 offset0:64 offset1:96
	v_mul_f32_e32 v0, v14, v38
	v_mul_f32_e32 v1, v30, v38
	ds_write2_b32 v2, v0, v1 offset0:128 offset1:160
	v_mul_f32_e32 v0, v15, v39
	v_mul_f32_e32 v1, v31, v39
	v_and_b32_e32 v8, 0xf0, v185
	ds_write2_b32 v2, v0, v1 offset0:192 offset1:224
	v_add_u32_e32 v14, s2, v8
	s_waitcnt lgkmcnt(0)
	v_lshl_add_u32 v0, v183, 8, v14
	v_or_b32_e32 v15, 4, v183
	s_lshl_b32 s3, s21, 2
	ds_read_b128 v[0:3], v0 offset:51200
	v_lshl_add_u32 v4, v15, 8, v14
	s_add_u32 s0, s0, s3
	ds_read_b128 v[4:7], v4 offset:51200
	s_addc_u32 s1, s1, 0
	v_mov_b32_e32 v9, 0
	v_lshl_add_u64 v[10:11], s[0:1], 0, v[8:9]
	v_lshlrev_b32_e32 v8, 11, v183
	v_lshl_add_u64 v[12:13], v[10:11], 0, v[8:9]
	v_lshlrev_b32_e32 v8, 11, v15
	s_waitcnt lgkmcnt(1)
	global_store_dwordx4 v[12:13], v[0:3], off sc1
	v_or_b32_e32 v15, 12, v183
	s_nop 0
	v_lshl_add_u64 v[0:1], v[10:11], 0, v[8:9]
	s_waitcnt lgkmcnt(0)
	global_store_dwordx4 v[0:1], v[4:7], off sc1
	s_nop 1
	v_or_b32_e32 v4, 8, v183
	v_lshl_add_u32 v0, v4, 8, v14
	ds_read_b128 v[0:3], v0 offset:51200
	v_lshlrev_b32_e32 v8, 11, v4
	v_lshl_add_u32 v4, v15, 8, v14
	ds_read_b128 v[4:7], v4 offset:51200
	v_lshl_add_u64 v[12:13], v[10:11], 0, v[8:9]
	v_lshlrev_b32_e32 v8, 11, v15
	s_waitcnt lgkmcnt(1)
	global_store_dwordx4 v[12:13], v[0:3], off sc1
	v_or_b32_e32 v15, 20, v183
	s_nop 0
	v_lshl_add_u64 v[0:1], v[10:11], 0, v[8:9]
	s_waitcnt lgkmcnt(0)
	global_store_dwordx4 v[0:1], v[4:7], off sc1
	s_nop 1
	v_or_b32_e32 v4, 16, v183
	v_lshl_add_u32 v0, v4, 8, v14
	ds_read_b128 v[0:3], v0 offset:51200
	v_lshlrev_b32_e32 v8, 11, v4
	v_lshl_add_u32 v4, v15, 8, v14
	ds_read_b128 v[4:7], v4 offset:51200
	v_lshl_add_u64 v[12:13], v[10:11], 0, v[8:9]
	v_lshlrev_b32_e32 v8, 11, v15
	s_waitcnt lgkmcnt(1)
	global_store_dwordx4 v[12:13], v[0:3], off sc1
	v_or_b32_e32 v15, 28, v183
	s_nop 0
	v_lshl_add_u64 v[0:1], v[10:11], 0, v[8:9]
	s_waitcnt lgkmcnt(0)
	global_store_dwordx4 v[0:1], v[4:7], off sc1
	s_nop 1
	v_or_b32_e32 v4, 24, v183
	v_lshl_add_u32 v0, v4, 8, v14
	ds_read_b128 v[0:3], v0 offset:51200
	v_lshlrev_b32_e32 v8, 11, v4
	v_lshl_add_u32 v4, v15, 8, v14
	ds_read_b128 v[4:7], v4 offset:51200
	v_lshl_add_u64 v[12:13], v[10:11], 0, v[8:9]
	v_lshlrev_b32_e32 v8, 11, v15
	s_waitcnt lgkmcnt(1)
	global_store_dwordx4 v[12:13], v[0:3], off sc1
	s_nop 1
	v_lshl_add_u64 v[0:1], v[10:11], 0, v[8:9]
	s_waitcnt lgkmcnt(0)
	global_store_dwordx4 v[0:1], v[4:7], off sc1
	s_endpgm
